# v57 + static priority (guide 7.4): all K-loop s_setprio flips deleted in the three GEMM loops, waves 4-7 raised to prio 1 once per unit, reset after the loop
# baseline (speedup 1.0000x reference)
.LBB0_264:
	s_ashr_i32 s73, s72, 31
	s_lshl_b64 s[26:27], s[72:73], 21
	s_add_u32 s76, s38, s26
	s_addc_u32 s77, s40, s27
	s_and_b64 s[26:27], s[4:5], exec
	s_cselect_b32 s73, s77, s7
	s_cselect_b32 vcc_lo, s76, s6
	s_ashr_i32 s75, s74, 31
	s_lshl_b64 s[26:27], s[74:75], 21
	s_add_u32 s96, s42, s26
	s_addc_u32 s97, s44, s27
	s_and_b64 s[26:27], s[4:5], exec
	s_cselect_b32 s75, s97, s25
	s_cselect_b32 vcc_hi, s96, s24
	s_add_u32 s6, s6, 0x100080
	s_addc_u32 s7, s7, 0
	s_add_u32 s21, s24, 0x100
	s_addc_u32 s13, s25, 0
	s_mov_b32 s58, -2
	s_cmp_eq_u64 s[30:31], 0
	s_cbranch_scc0 .Lsprio_ip
	s_setprio 1
.Lsprio_ip:
	s_add_u32 s24, s6, 0xfff00080
	s_addc_u32 s25, s7, -1
	s_add_i32 s28, 0, 0x10000
	s_cmp_eq_u32 s58, 60
	s_cselect_b32 s27, s73, s25
	s_cselect_b32 s26, vcc_lo, s24
	s_cselect_b32 s25, s75, s13
	s_cselect_b32 s24, vcc_hi, s21
	s_add_i32 s71, 0, 0x14000
	v_add_u32_e32 v144, s28, v163
	v_add_u32_e32 v182, s71, v163
	s_waitcnt lgkmcnt(0)
	ds_read_b128 v[132:135], v144
	ds_read_b128 v[136:139], v144 offset:1024
	ds_read_b128 v[140:143], v144 offset:2048
	ds_read_b128 v[144:147], v144 offset:3072
	ds_read_b128 v[148:151], v182
	ds_read_b128 v[152:155], v182 offset:1024
	ds_read_b128 v[178:181], v182 offset:2048
	ds_read_b128 v[186:189], v182 offset:3072
	v_lshl_add_u64 v[182:183], s[6:7], 0, v[174:175]
	s_add_i32 m0, s46, 0xc000
	ds_read_b128 v[190:193], v184
	ds_read_b128 v[194:197], v184 offset:1024
	ds_read_b128 v[198:201], v184 offset:2048
	ds_read_b128 v[202:205], v184 offset:3072
	ds_read_b128 v[222:225], v184 offset:4096
	ds_read_b128 v[226:229], v184 offset:5120
	ds_read_b128 v[230:233], v184 offset:6144
	ds_read_b128 v[234:237], v184 offset:7168
	global_load_lds_dwordx4 v[182:183], off
	v_lshl_add_u64 v[182:183], s[6:7], 0, v[176:177]
	s_add_i32 m0, s46, 0xe000
	s_nop 0
	global_load_lds_dwordx4 v[182:183], off
	s_waitcnt vmcnt(8)
	s_waitcnt lgkmcnt(0)
	s_barrier
	v_mfma_f32_16x16x32_bf16 v[120:123], v[132:135], v[190:193], 0
	v_mfma_f32_16x16x32_bf16 v[116:119], v[140:143], v[190:193], 0
	v_mfma_f32_16x16x32_bf16 v[104:107], v[132:135], v[198:201], 0
	v_mfma_f32_16x16x32_bf16 v[100:103], v[140:143], v[198:201], 0
	v_mfma_f32_16x16x32_bf16 v[88:91], v[132:135], v[222:225], 0
	v_mfma_f32_16x16x32_bf16 v[84:87], v[140:143], v[222:225], 0
	v_mfma_f32_16x16x32_bf16 v[72:75], v[132:135], v[230:233], 0
	v_mfma_f32_16x16x32_bf16 v[68:71], v[140:143], v[230:233], 0
	v_mfma_f32_16x16x32_bf16 v[120:123], v[136:139], v[194:197], v[120:123]
	v_mfma_f32_16x16x32_bf16 v[116:119], v[144:147], v[194:197], v[116:119]
	v_mfma_f32_16x16x32_bf16 v[104:107], v[136:139], v[202:205], v[104:107]
	v_mfma_f32_16x16x32_bf16 v[100:103], v[144:147], v[202:205], v[100:103]
	v_mfma_f32_16x16x32_bf16 v[88:91], v[136:139], v[226:229], v[88:91]
	v_mfma_f32_16x16x32_bf16 v[84:87], v[144:147], v[226:229], v[84:87]
	v_mfma_f32_16x16x32_bf16 v[72:75], v[136:139], v[234:237], v[72:75]
	v_mfma_f32_16x16x32_bf16 v[68:71], v[144:147], v[234:237], v[68:71]
	v_mfma_f32_16x16x32_bf16 v[128:131], v[148:151], v[190:193], 0
	v_mfma_f32_16x16x32_bf16 v[124:127], v[178:181], v[190:193], 0
	v_mfma_f32_16x16x32_bf16 v[112:115], v[148:151], v[198:201], 0
	v_mfma_f32_16x16x32_bf16 v[108:111], v[178:181], v[198:201], 0
	v_mfma_f32_16x16x32_bf16 v[96:99], v[148:151], v[222:225], 0
	v_mfma_f32_16x16x32_bf16 v[92:95], v[178:181], v[222:225], 0
	v_mfma_f32_16x16x32_bf16 v[80:83], v[148:151], v[230:233], 0
	v_mfma_f32_16x16x32_bf16 v[76:79], v[178:181], v[230:233], 0
	v_mfma_f32_16x16x32_bf16 v[128:131], v[152:155], v[194:197], v[128:131]
	v_mfma_f32_16x16x32_bf16 v[124:127], v[186:189], v[194:197], v[124:127]
	v_mfma_f32_16x16x32_bf16 v[112:115], v[152:155], v[202:205], v[112:115]
	v_mfma_f32_16x16x32_bf16 v[108:111], v[186:189], v[202:205], v[108:111]
	v_mfma_f32_16x16x32_bf16 v[96:99], v[152:155], v[226:229], v[96:99]
	v_mfma_f32_16x16x32_bf16 v[92:95], v[186:189], v[226:229], v[92:95]
	v_mfma_f32_16x16x32_bf16 v[80:83], v[152:155], v[234:237], v[80:83]
	v_mfma_f32_16x16x32_bf16 v[76:79], v[186:189], v[234:237], v[76:79]
	s_barrier
	s_add_i32 s28, s28, s1
	v_lshl_add_u64 v[182:183], s[24:25], 0, v[2:3]
	s_mov_b32 m0, s28
	ds_read_b128 v[190:193], v184 offset:16384
	ds_read_b128 v[194:197], v184 offset:17408
	ds_read_b128 v[198:201], v184 offset:18432
	ds_read_b128 v[202:205], v184 offset:19456
	ds_read_b128 v[222:225], v184 offset:20480
	ds_read_b128 v[226:229], v184 offset:21504
	ds_read_b128 v[230:233], v184 offset:22528
	ds_read_b128 v[234:237], v184 offset:23552
	global_load_lds_dwordx4 v[182:183], off
	s_add_i32 m0, s28, 0x2000
	s_add_u32 s28, s24, 0x100000
	v_lshl_add_u64 v[238:239], s[24:25], 0, v[168:169]
	s_addc_u32 s29, s25, 0
	s_add_i32 s71, s71, s1
	global_load_lds_dwordx4 v[238:239], off
	v_lshl_add_u64 v[240:241], s[28:29], 0, v[2:3]
	s_mov_b32 m0, s71
	v_lshl_add_u64 v[242:243], s[26:27], 0, v[170:171]
	global_load_lds_dwordx4 v[240:241], off
	v_lshl_add_u64 v[240:241], s[28:29], 0, v[168:169]
	s_add_i32 m0, s71, 0x2000
	s_nop 0
	global_load_lds_dwordx4 v[240:241], off
	v_lshl_add_u64 v[240:241], s[26:27], 0, v[172:173]
	s_mov_b32 m0, s46
	s_nop 0
	global_load_lds_dwordx4 v[240:241], off
	s_mov_b32 m0, s50
	s_nop 0
	global_load_lds_dwordx4 v[242:243], off
	s_waitcnt vmcnt(8)
	s_waitcnt lgkmcnt(0)
	s_barrier
	v_mfma_f32_16x16x32_bf16 v[56:59], v[132:135], v[190:193], 0
	v_mfma_f32_16x16x32_bf16 v[52:55], v[140:143], v[190:193], 0
	v_mfma_f32_16x16x32_bf16 v[40:43], v[132:135], v[198:201], 0
	v_mfma_f32_16x16x32_bf16 v[36:39], v[140:143], v[198:201], 0
	v_mfma_f32_16x16x32_bf16 v[24:27], v[132:135], v[222:225], 0
	v_mfma_f32_16x16x32_bf16 v[20:23], v[140:143], v[222:225], 0
	v_mfma_f32_16x16x32_bf16 v[8:11], v[132:135], v[230:233], 0
	v_mfma_f32_16x16x32_bf16 v[4:7], v[140:143], v[230:233], 0
	v_mfma_f32_16x16x32_bf16 v[56:59], v[136:139], v[194:197], v[56:59]
	v_mfma_f32_16x16x32_bf16 v[52:55], v[144:147], v[194:197], v[52:55]
	v_mfma_f32_16x16x32_bf16 v[40:43], v[136:139], v[202:205], v[40:43]
	v_mfma_f32_16x16x32_bf16 v[36:39], v[144:147], v[202:205], v[36:39]
	v_mfma_f32_16x16x32_bf16 v[24:27], v[136:139], v[226:229], v[24:27]
	v_mfma_f32_16x16x32_bf16 v[20:23], v[144:147], v[226:229], v[20:23]
	v_mfma_f32_16x16x32_bf16 v[8:11], v[136:139], v[234:237], v[8:11]
	v_mfma_f32_16x16x32_bf16 v[4:7], v[144:147], v[234:237], v[4:7]
	v_mfma_f32_16x16x32_bf16 v[64:67], v[148:151], v[190:193], 0
	v_mfma_f32_16x16x32_bf16 v[60:63], v[178:181], v[190:193], 0
	v_mfma_f32_16x16x32_bf16 v[48:51], v[148:151], v[198:201], 0
	v_mfma_f32_16x16x32_bf16 v[44:47], v[178:181], v[198:201], 0
	v_mfma_f32_16x16x32_bf16 v[32:35], v[148:151], v[222:225], 0
	v_mfma_f32_16x16x32_bf16 v[28:31], v[178:181], v[222:225], 0
	v_mfma_f32_16x16x32_bf16 v[16:19], v[148:151], v[230:233], 0
	v_mfma_f32_16x16x32_bf16 v[12:15], v[178:181], v[230:233], 0
	v_mfma_f32_16x16x32_bf16 v[64:67], v[152:155], v[194:197], v[64:67]
	v_mfma_f32_16x16x32_bf16 v[60:63], v[186:189], v[194:197], v[60:63]
	v_mfma_f32_16x16x32_bf16 v[48:51], v[152:155], v[202:205], v[48:51]
	v_mfma_f32_16x16x32_bf16 v[44:47], v[186:189], v[202:205], v[44:47]
	v_mfma_f32_16x16x32_bf16 v[32:35], v[152:155], v[226:229], v[32:35]
	v_mfma_f32_16x16x32_bf16 v[28:31], v[186:189], v[226:229], v[28:31]
	v_mfma_f32_16x16x32_bf16 v[16:19], v[152:155], v[234:237], v[16:19]
	v_mfma_f32_16x16x32_bf16 v[12:15], v[186:189], v[234:237], v[12:15]
	s_barrier
	s_add_i32 s28, 0, 0x18000
	s_add_i32 s29, 0, 0x1c000
	v_add_u32_e32 v144, s28, v163
	v_add_u32_e32 v185, s29, v163
	ds_read_b128 v[132:135], v144
	ds_read_b128 v[136:139], v144 offset:1024
	ds_read_b128 v[140:143], v144 offset:2048
	ds_read_b128 v[144:147], v144 offset:3072
	ds_read_b128 v[148:151], v185
	ds_read_b128 v[152:155], v185 offset:1024
	ds_read_b128 v[178:181], v185 offset:2048
	ds_read_b128 v[186:189], v185 offset:3072
	s_add_u32 s26, s26, 0x100000
	s_addc_u32 s27, s27, 0
	s_mov_b32 m0, s51
	v_lshl_add_u64 v[244:245], s[26:27], 0, v[172:173]
	ds_read_b128 v[190:193], v184 offset:32768
	ds_read_b128 v[194:197], v184 offset:33792
	ds_read_b128 v[198:201], v184 offset:34816
	ds_read_b128 v[202:205], v184 offset:35840
	ds_read_b128 v[222:225], v184 offset:36864
	ds_read_b128 v[226:229], v184 offset:37888
	ds_read_b128 v[230:233], v184 offset:38912
	ds_read_b128 v[234:237], v184 offset:39936
	global_load_lds_dwordx4 v[244:245], off
	v_lshl_add_u64 v[244:245], s[26:27], 0, v[170:171]
	s_mov_b32 m0, s54
	s_nop 0
	global_load_lds_dwordx4 v[244:245], off
	s_waitcnt vmcnt(8)
	s_waitcnt lgkmcnt(0)
	s_barrier
	v_mfma_f32_16x16x32_bf16 v[120:123], v[132:135], v[190:193], v[120:123]
	v_mfma_f32_16x16x32_bf16 v[116:119], v[140:143], v[190:193], v[116:119]
	v_mfma_f32_16x16x32_bf16 v[104:107], v[132:135], v[198:201], v[104:107]
	v_mfma_f32_16x16x32_bf16 v[100:103], v[140:143], v[198:201], v[100:103]
	v_mfma_f32_16x16x32_bf16 v[88:91], v[132:135], v[222:225], v[88:91]
	v_mfma_f32_16x16x32_bf16 v[84:87], v[140:143], v[222:225], v[84:87]
	v_mfma_f32_16x16x32_bf16 v[72:75], v[132:135], v[230:233], v[72:75]
	v_mfma_f32_16x16x32_bf16 v[68:71], v[140:143], v[230:233], v[68:71]
	v_mfma_f32_16x16x32_bf16 v[120:123], v[136:139], v[194:197], v[120:123]
	v_mfma_f32_16x16x32_bf16 v[116:119], v[144:147], v[194:197], v[116:119]
	v_mfma_f32_16x16x32_bf16 v[104:107], v[136:139], v[202:205], v[104:107]
	v_mfma_f32_16x16x32_bf16 v[100:103], v[144:147], v[202:205], v[100:103]
	v_mfma_f32_16x16x32_bf16 v[88:91], v[136:139], v[226:229], v[88:91]
	v_mfma_f32_16x16x32_bf16 v[84:87], v[144:147], v[226:229], v[84:87]
	v_mfma_f32_16x16x32_bf16 v[72:75], v[136:139], v[234:237], v[72:75]
	v_mfma_f32_16x16x32_bf16 v[68:71], v[144:147], v[234:237], v[68:71]
	v_mfma_f32_16x16x32_bf16 v[128:131], v[148:151], v[190:193], v[128:131]
	v_mfma_f32_16x16x32_bf16 v[124:127], v[178:181], v[190:193], v[124:127]
	v_mfma_f32_16x16x32_bf16 v[112:115], v[148:151], v[198:201], v[112:115]
	v_mfma_f32_16x16x32_bf16 v[108:111], v[178:181], v[198:201], v[108:111]
	v_mfma_f32_16x16x32_bf16 v[96:99], v[148:151], v[222:225], v[96:99]
	v_mfma_f32_16x16x32_bf16 v[92:95], v[178:181], v[222:225], v[92:95]
	v_mfma_f32_16x16x32_bf16 v[80:83], v[148:151], v[230:233], v[80:83]
	v_mfma_f32_16x16x32_bf16 v[76:79], v[178:181], v[230:233], v[76:79]
	v_mfma_f32_16x16x32_bf16 v[128:131], v[152:155], v[194:197], v[128:131]
	v_mfma_f32_16x16x32_bf16 v[124:127], v[186:189], v[194:197], v[124:127]
	v_mfma_f32_16x16x32_bf16 v[112:115], v[152:155], v[202:205], v[112:115]
	v_mfma_f32_16x16x32_bf16 v[108:111], v[186:189], v[202:205], v[108:111]
	v_mfma_f32_16x16x32_bf16 v[96:99], v[152:155], v[226:229], v[96:99]
	v_mfma_f32_16x16x32_bf16 v[92:95], v[186:189], v[226:229], v[92:95]
	v_mfma_f32_16x16x32_bf16 v[80:83], v[152:155], v[234:237], v[80:83]
	v_mfma_f32_16x16x32_bf16 v[76:79], v[186:189], v[234:237], v[76:79]
	s_barrier
	s_add_i32 s26, s28, s1
	v_lshl_add_u64 v[182:183], v[182:183], 0, s[86:87]
	s_mov_b32 m0, s26
	ds_read_b128 v[190:193], v184 offset:49152
	ds_read_b128 v[194:197], v184 offset:50176
	ds_read_b128 v[198:201], v184 offset:51200
	ds_read_b128 v[202:205], v184 offset:52224
	ds_read_b128 v[222:225], v184 offset:53248
	ds_read_b128 v[226:229], v184 offset:54272
	ds_read_b128 v[230:233], v184 offset:55296
	ds_read_b128 v[234:237], v184 offset:56320
	global_load_lds_dwordx4 v[182:183], off
	s_add_i32 m0, s26, 0x2000
	s_add_u32 s24, s24, 0x100080
	v_lshl_add_u64 v[182:183], v[238:239], 0, s[86:87]
	s_addc_u32 s25, s25, 0
	s_add_i32 s26, s29, s1
	global_load_lds_dwordx4 v[182:183], off
	v_lshl_add_u64 v[182:183], s[24:25], 0, v[2:3]
	s_mov_b32 m0, s26
	s_nop 0
	global_load_lds_dwordx4 v[182:183], off
	v_lshl_add_u64 v[182:183], s[24:25], 0, v[168:169]
	s_add_i32 m0, s26, 0x2000
	s_nop 0
	global_load_lds_dwordx4 v[182:183], off
	v_lshl_add_u64 v[182:183], v[240:241], 0, s[86:87]
	s_mov_b32 m0, s78
	s_nop 0
	global_load_lds_dwordx4 v[182:183], off
	v_lshl_add_u64 v[182:183], v[242:243], 0, s[86:87]
	s_mov_b32 m0, s85
	s_nop 0
	global_load_lds_dwordx4 v[182:183], off
	s_waitcnt vmcnt(8)
	s_waitcnt lgkmcnt(0)
	s_barrier
	v_mfma_f32_16x16x32_bf16 v[56:59], v[132:135], v[190:193], v[56:59]
	v_mfma_f32_16x16x32_bf16 v[52:55], v[140:143], v[190:193], v[52:55]
	v_mfma_f32_16x16x32_bf16 v[40:43], v[132:135], v[198:201], v[40:43]
	v_mfma_f32_16x16x32_bf16 v[36:39], v[140:143], v[198:201], v[36:39]
	v_mfma_f32_16x16x32_bf16 v[24:27], v[132:135], v[222:225], v[24:27]
	v_mfma_f32_16x16x32_bf16 v[20:23], v[140:143], v[222:225], v[20:23]
	v_mfma_f32_16x16x32_bf16 v[8:11], v[132:135], v[230:233], v[8:11]
	v_mfma_f32_16x16x32_bf16 v[4:7], v[140:143], v[230:233], v[4:7]
	v_mfma_f32_16x16x32_bf16 v[56:59], v[136:139], v[194:197], v[56:59]
	v_mfma_f32_16x16x32_bf16 v[52:55], v[144:147], v[194:197], v[52:55]
	v_mfma_f32_16x16x32_bf16 v[40:43], v[136:139], v[202:205], v[40:43]
	v_mfma_f32_16x16x32_bf16 v[36:39], v[144:147], v[202:205], v[36:39]
	v_mfma_f32_16x16x32_bf16 v[24:27], v[136:139], v[226:229], v[24:27]
	v_mfma_f32_16x16x32_bf16 v[20:23], v[144:147], v[226:229], v[20:23]
	v_mfma_f32_16x16x32_bf16 v[8:11], v[136:139], v[234:237], v[8:11]
	v_mfma_f32_16x16x32_bf16 v[4:7], v[144:147], v[234:237], v[4:7]
	v_mfma_f32_16x16x32_bf16 v[64:67], v[148:151], v[190:193], v[64:67]
	v_mfma_f32_16x16x32_bf16 v[60:63], v[178:181], v[190:193], v[60:63]
	v_mfma_f32_16x16x32_bf16 v[48:51], v[148:151], v[198:201], v[48:51]
	v_mfma_f32_16x16x32_bf16 v[44:47], v[178:181], v[198:201], v[44:47]
	v_mfma_f32_16x16x32_bf16 v[32:35], v[148:151], v[222:225], v[32:35]
	v_mfma_f32_16x16x32_bf16 v[28:31], v[178:181], v[222:225], v[28:31]
	v_mfma_f32_16x16x32_bf16 v[16:19], v[148:151], v[230:233], v[16:19]
	v_mfma_f32_16x16x32_bf16 v[12:15], v[178:181], v[230:233], v[12:15]
	v_mfma_f32_16x16x32_bf16 v[64:67], v[152:155], v[194:197], v[64:67]
	v_mfma_f32_16x16x32_bf16 v[60:63], v[186:189], v[194:197], v[60:63]
	v_mfma_f32_16x16x32_bf16 v[48:51], v[152:155], v[202:205], v[48:51]
	v_mfma_f32_16x16x32_bf16 v[44:47], v[186:189], v[202:205], v[44:47]
	v_mfma_f32_16x16x32_bf16 v[32:35], v[152:155], v[226:229], v[32:35]
	v_mfma_f32_16x16x32_bf16 v[28:31], v[186:189], v[226:229], v[28:31]
	v_mfma_f32_16x16x32_bf16 v[16:19], v[152:155], v[234:237], v[16:19]
	v_mfma_f32_16x16x32_bf16 v[12:15], v[186:189], v[234:237], v[12:15]
	s_barrier
	s_add_i32 s58, s58, 2
	s_add_u32 s6, s6, 0x100
	s_addc_u32 s7, s7, 0
	s_add_u32 s21, s21, 0x100
	s_addc_u32 s13, s13, 0
	s_cmp_gt_u32 s58, 61
	s_cbranch_scc0 .LBB0_265
.LBB0_265:
	s_add_u32 s24, s6, 0xfff00080
	s_addc_u32 s25, s7, -1
	s_add_i32 s28, 0, 0x10000
	s_cmp_eq_u32 s58, 60
	s_cselect_b32 s27, s73, s25
	s_cselect_b32 s26, vcc_lo, s24
	s_cselect_b32 s25, s75, s13
	s_cselect_b32 s24, vcc_hi, s21
	s_add_i32 s71, 0, 0x14000
	v_add_u32_e32 v144, s28, v163
	v_add_u32_e32 v182, s71, v163
	s_waitcnt lgkmcnt(0)
	ds_read_b128 v[132:135], v144
	ds_read_b128 v[136:139], v144 offset:1024
	ds_read_b128 v[140:143], v144 offset:2048
	ds_read_b128 v[144:147], v144 offset:3072
	ds_read_b128 v[148:151], v182
	ds_read_b128 v[152:155], v182 offset:1024
	ds_read_b128 v[178:181], v182 offset:2048
	ds_read_b128 v[186:189], v182 offset:3072
	v_lshl_add_u64 v[182:183], s[6:7], 0, v[174:175]
	s_add_i32 m0, s46, 0xc000
	ds_read_b128 v[190:193], v184
	ds_read_b128 v[194:197], v184 offset:1024
	ds_read_b128 v[198:201], v184 offset:2048
	ds_read_b128 v[202:205], v184 offset:3072
	ds_read_b128 v[222:225], v184 offset:4096
	ds_read_b128 v[226:229], v184 offset:5120
	ds_read_b128 v[230:233], v184 offset:6144
	ds_read_b128 v[234:237], v184 offset:7168
	global_load_lds_dwordx4 v[182:183], off
	v_lshl_add_u64 v[182:183], s[6:7], 0, v[176:177]
	s_add_i32 m0, s46, 0xe000
	s_nop 0
	global_load_lds_dwordx4 v[182:183], off
	s_waitcnt vmcnt(8)
	s_waitcnt lgkmcnt(0)
	s_barrier
	v_mfma_f32_16x16x32_bf16 v[120:123], v[132:135], v[190:193], v[120:123]
	v_mfma_f32_16x16x32_bf16 v[116:119], v[140:143], v[190:193], v[116:119]
	v_mfma_f32_16x16x32_bf16 v[104:107], v[132:135], v[198:201], v[104:107]
	v_mfma_f32_16x16x32_bf16 v[100:103], v[140:143], v[198:201], v[100:103]
	v_mfma_f32_16x16x32_bf16 v[88:91], v[132:135], v[222:225], v[88:91]
	v_mfma_f32_16x16x32_bf16 v[84:87], v[140:143], v[222:225], v[84:87]
	v_mfma_f32_16x16x32_bf16 v[72:75], v[132:135], v[230:233], v[72:75]
	v_mfma_f32_16x16x32_bf16 v[68:71], v[140:143], v[230:233], v[68:71]
	v_mfma_f32_16x16x32_bf16 v[120:123], v[136:139], v[194:197], v[120:123]
	v_mfma_f32_16x16x32_bf16 v[116:119], v[144:147], v[194:197], v[116:119]
	v_mfma_f32_16x16x32_bf16 v[104:107], v[136:139], v[202:205], v[104:107]
	v_mfma_f32_16x16x32_bf16 v[100:103], v[144:147], v[202:205], v[100:103]
	v_mfma_f32_16x16x32_bf16 v[88:91], v[136:139], v[226:229], v[88:91]
	v_mfma_f32_16x16x32_bf16 v[84:87], v[144:147], v[226:229], v[84:87]
	v_mfma_f32_16x16x32_bf16 v[72:75], v[136:139], v[234:237], v[72:75]
	v_mfma_f32_16x16x32_bf16 v[68:71], v[144:147], v[234:237], v[68:71]
	v_mfma_f32_16x16x32_bf16 v[128:131], v[148:151], v[190:193], v[128:131]
	v_mfma_f32_16x16x32_bf16 v[124:127], v[178:181], v[190:193], v[124:127]
	v_mfma_f32_16x16x32_bf16 v[112:115], v[148:151], v[198:201], v[112:115]
	v_mfma_f32_16x16x32_bf16 v[108:111], v[178:181], v[198:201], v[108:111]
	v_mfma_f32_16x16x32_bf16 v[96:99], v[148:151], v[222:225], v[96:99]
	v_mfma_f32_16x16x32_bf16 v[92:95], v[178:181], v[222:225], v[92:95]
	v_mfma_f32_16x16x32_bf16 v[80:83], v[148:151], v[230:233], v[80:83]
	v_mfma_f32_16x16x32_bf16 v[76:79], v[178:181], v[230:233], v[76:79]
	v_mfma_f32_16x16x32_bf16 v[128:131], v[152:155], v[194:197], v[128:131]
	v_mfma_f32_16x16x32_bf16 v[124:127], v[186:189], v[194:197], v[124:127]
	v_mfma_f32_16x16x32_bf16 v[112:115], v[152:155], v[202:205], v[112:115]
	v_mfma_f32_16x16x32_bf16 v[108:111], v[186:189], v[202:205], v[108:111]
	v_mfma_f32_16x16x32_bf16 v[96:99], v[152:155], v[226:229], v[96:99]
	v_mfma_f32_16x16x32_bf16 v[92:95], v[186:189], v[226:229], v[92:95]
	v_mfma_f32_16x16x32_bf16 v[80:83], v[152:155], v[234:237], v[80:83]
	v_mfma_f32_16x16x32_bf16 v[76:79], v[186:189], v[234:237], v[76:79]
	s_barrier
	s_add_i32 s28, s28, s1
	v_lshl_add_u64 v[182:183], s[24:25], 0, v[2:3]
	s_mov_b32 m0, s28
	ds_read_b128 v[190:193], v184 offset:16384
	ds_read_b128 v[194:197], v184 offset:17408
	ds_read_b128 v[198:201], v184 offset:18432
	ds_read_b128 v[202:205], v184 offset:19456
	ds_read_b128 v[222:225], v184 offset:20480
	ds_read_b128 v[226:229], v184 offset:21504
	ds_read_b128 v[230:233], v184 offset:22528
	ds_read_b128 v[234:237], v184 offset:23552
	global_load_lds_dwordx4 v[182:183], off
	s_add_i32 m0, s28, 0x2000
	s_add_u32 s28, s24, 0x100000
	v_lshl_add_u64 v[238:239], s[24:25], 0, v[168:169]
	s_addc_u32 s29, s25, 0
	s_add_i32 s71, s71, s1
	global_load_lds_dwordx4 v[238:239], off
	v_lshl_add_u64 v[240:241], s[28:29], 0, v[2:3]
	s_mov_b32 m0, s71
	v_lshl_add_u64 v[242:243], s[26:27], 0, v[170:171]
	global_load_lds_dwordx4 v[240:241], off
	v_lshl_add_u64 v[240:241], s[28:29], 0, v[168:169]
	s_add_i32 m0, s71, 0x2000
	s_nop 0
	global_load_lds_dwordx4 v[240:241], off
	v_lshl_add_u64 v[240:241], s[26:27], 0, v[172:173]
	s_mov_b32 m0, s46
	s_nop 0
	global_load_lds_dwordx4 v[240:241], off
	s_mov_b32 m0, s50
	s_nop 0
	global_load_lds_dwordx4 v[242:243], off
	s_waitcnt vmcnt(8)
	s_waitcnt lgkmcnt(0)
	s_barrier
	v_mfma_f32_16x16x32_bf16 v[56:59], v[132:135], v[190:193], v[56:59]
	v_mfma_f32_16x16x32_bf16 v[52:55], v[140:143], v[190:193], v[52:55]
	v_mfma_f32_16x16x32_bf16 v[40:43], v[132:135], v[198:201], v[40:43]
	v_mfma_f32_16x16x32_bf16 v[36:39], v[140:143], v[198:201], v[36:39]
	v_mfma_f32_16x16x32_bf16 v[24:27], v[132:135], v[222:225], v[24:27]
	v_mfma_f32_16x16x32_bf16 v[20:23], v[140:143], v[222:225], v[20:23]
	v_mfma_f32_16x16x32_bf16 v[8:11], v[132:135], v[230:233], v[8:11]
	v_mfma_f32_16x16x32_bf16 v[4:7], v[140:143], v[230:233], v[4:7]
	v_mfma_f32_16x16x32_bf16 v[56:59], v[136:139], v[194:197], v[56:59]
	v_mfma_f32_16x16x32_bf16 v[52:55], v[144:147], v[194:197], v[52:55]
	v_mfma_f32_16x16x32_bf16 v[40:43], v[136:139], v[202:205], v[40:43]
	v_mfma_f32_16x16x32_bf16 v[36:39], v[144:147], v[202:205], v[36:39]
	v_mfma_f32_16x16x32_bf16 v[24:27], v[136:139], v[226:229], v[24:27]
	v_mfma_f32_16x16x32_bf16 v[20:23], v[144:147], v[226:229], v[20:23]
	v_mfma_f32_16x16x32_bf16 v[8:11], v[136:139], v[234:237], v[8:11]
	v_mfma_f32_16x16x32_bf16 v[4:7], v[144:147], v[234:237], v[4:7]
	v_mfma_f32_16x16x32_bf16 v[64:67], v[148:151], v[190:193], v[64:67]
	v_mfma_f32_16x16x32_bf16 v[60:63], v[178:181], v[190:193], v[60:63]
	v_mfma_f32_16x16x32_bf16 v[48:51], v[148:151], v[198:201], v[48:51]
	v_mfma_f32_16x16x32_bf16 v[44:47], v[178:181], v[198:201], v[44:47]
	v_mfma_f32_16x16x32_bf16 v[32:35], v[148:151], v[222:225], v[32:35]
	v_mfma_f32_16x16x32_bf16 v[28:31], v[178:181], v[222:225], v[28:31]
	v_mfma_f32_16x16x32_bf16 v[16:19], v[148:151], v[230:233], v[16:19]
	v_mfma_f32_16x16x32_bf16 v[12:15], v[178:181], v[230:233], v[12:15]
	v_mfma_f32_16x16x32_bf16 v[64:67], v[152:155], v[194:197], v[64:67]
	v_mfma_f32_16x16x32_bf16 v[60:63], v[186:189], v[194:197], v[60:63]
	v_mfma_f32_16x16x32_bf16 v[48:51], v[152:155], v[202:205], v[48:51]
	v_mfma_f32_16x16x32_bf16 v[44:47], v[186:189], v[202:205], v[44:47]
	v_mfma_f32_16x16x32_bf16 v[32:35], v[152:155], v[226:229], v[32:35]
	v_mfma_f32_16x16x32_bf16 v[28:31], v[186:189], v[226:229], v[28:31]
	v_mfma_f32_16x16x32_bf16 v[16:19], v[152:155], v[234:237], v[16:19]
	v_mfma_f32_16x16x32_bf16 v[12:15], v[186:189], v[234:237], v[12:15]
	s_barrier
	s_add_i32 s28, 0, 0x18000
	s_add_i32 s29, 0, 0x1c000
	v_add_u32_e32 v144, s28, v163
	v_add_u32_e32 v185, s29, v163
	ds_read_b128 v[132:135], v144
	ds_read_b128 v[136:139], v144 offset:1024
	ds_read_b128 v[140:143], v144 offset:2048
	ds_read_b128 v[144:147], v144 offset:3072
	ds_read_b128 v[148:151], v185
	ds_read_b128 v[152:155], v185 offset:1024
	ds_read_b128 v[178:181], v185 offset:2048
	ds_read_b128 v[186:189], v185 offset:3072
	s_add_u32 s26, s26, 0x100000
	s_addc_u32 s27, s27, 0
	s_mov_b32 m0, s51
	v_lshl_add_u64 v[244:245], s[26:27], 0, v[172:173]
	ds_read_b128 v[190:193], v184 offset:32768
	ds_read_b128 v[194:197], v184 offset:33792
	ds_read_b128 v[198:201], v184 offset:34816
	ds_read_b128 v[202:205], v184 offset:35840
	ds_read_b128 v[222:225], v184 offset:36864
	ds_read_b128 v[226:229], v184 offset:37888
	ds_read_b128 v[230:233], v184 offset:38912
	ds_read_b128 v[234:237], v184 offset:39936
	global_load_lds_dwordx4 v[244:245], off
	v_lshl_add_u64 v[244:245], s[26:27], 0, v[170:171]
	s_mov_b32 m0, s54
	s_nop 0
	global_load_lds_dwordx4 v[244:245], off
	s_waitcnt vmcnt(8)
	s_waitcnt lgkmcnt(0)
	s_barrier
	v_mfma_f32_16x16x32_bf16 v[120:123], v[132:135], v[190:193], v[120:123]
	v_mfma_f32_16x16x32_bf16 v[116:119], v[140:143], v[190:193], v[116:119]
	v_mfma_f32_16x16x32_bf16 v[104:107], v[132:135], v[198:201], v[104:107]
	v_mfma_f32_16x16x32_bf16 v[100:103], v[140:143], v[198:201], v[100:103]
	v_mfma_f32_16x16x32_bf16 v[88:91], v[132:135], v[222:225], v[88:91]
	v_mfma_f32_16x16x32_bf16 v[84:87], v[140:143], v[222:225], v[84:87]
	v_mfma_f32_16x16x32_bf16 v[72:75], v[132:135], v[230:233], v[72:75]
	v_mfma_f32_16x16x32_bf16 v[68:71], v[140:143], v[230:233], v[68:71]
	v_mfma_f32_16x16x32_bf16 v[120:123], v[136:139], v[194:197], v[120:123]
	v_mfma_f32_16x16x32_bf16 v[116:119], v[144:147], v[194:197], v[116:119]
	v_mfma_f32_16x16x32_bf16 v[104:107], v[136:139], v[202:205], v[104:107]
	v_mfma_f32_16x16x32_bf16 v[100:103], v[144:147], v[202:205], v[100:103]
	v_mfma_f32_16x16x32_bf16 v[88:91], v[136:139], v[226:229], v[88:91]
	v_mfma_f32_16x16x32_bf16 v[84:87], v[144:147], v[226:229], v[84:87]
	v_mfma_f32_16x16x32_bf16 v[72:75], v[136:139], v[234:237], v[72:75]
	v_mfma_f32_16x16x32_bf16 v[68:71], v[144:147], v[234:237], v[68:71]
	v_mfma_f32_16x16x32_bf16 v[128:131], v[148:151], v[190:193], v[128:131]
	v_mfma_f32_16x16x32_bf16 v[124:127], v[178:181], v[190:193], v[124:127]
	v_mfma_f32_16x16x32_bf16 v[112:115], v[148:151], v[198:201], v[112:115]
	v_mfma_f32_16x16x32_bf16 v[108:111], v[178:181], v[198:201], v[108:111]
	v_mfma_f32_16x16x32_bf16 v[96:99], v[148:151], v[222:225], v[96:99]
	v_mfma_f32_16x16x32_bf16 v[92:95], v[178:181], v[222:225], v[92:95]
	v_mfma_f32_16x16x32_bf16 v[80:83], v[148:151], v[230:233], v[80:83]
	v_mfma_f32_16x16x32_bf16 v[76:79], v[178:181], v[230:233], v[76:79]
	v_mfma_f32_16x16x32_bf16 v[128:131], v[152:155], v[194:197], v[128:131]
	v_mfma_f32_16x16x32_bf16 v[124:127], v[186:189], v[194:197], v[124:127]
	v_mfma_f32_16x16x32_bf16 v[112:115], v[152:155], v[202:205], v[112:115]
	v_mfma_f32_16x16x32_bf16 v[108:111], v[186:189], v[202:205], v[108:111]
	v_mfma_f32_16x16x32_bf16 v[96:99], v[152:155], v[226:229], v[96:99]
	v_mfma_f32_16x16x32_bf16 v[92:95], v[186:189], v[226:229], v[92:95]
	v_mfma_f32_16x16x32_bf16 v[80:83], v[152:155], v[234:237], v[80:83]
	v_mfma_f32_16x16x32_bf16 v[76:79], v[186:189], v[234:237], v[76:79]
	s_barrier
	s_add_i32 s26, s28, s1
	v_lshl_add_u64 v[182:183], v[182:183], 0, s[86:87]
	s_mov_b32 m0, s26
	ds_read_b128 v[190:193], v184 offset:49152
	ds_read_b128 v[194:197], v184 offset:50176
	ds_read_b128 v[198:201], v184 offset:51200
	ds_read_b128 v[202:205], v184 offset:52224
	ds_read_b128 v[222:225], v184 offset:53248
	ds_read_b128 v[226:229], v184 offset:54272
	ds_read_b128 v[230:233], v184 offset:55296
	ds_read_b128 v[234:237], v184 offset:56320
	global_load_lds_dwordx4 v[182:183], off
	s_add_i32 m0, s26, 0x2000
	s_add_u32 s24, s24, 0x100080
	v_lshl_add_u64 v[182:183], v[238:239], 0, s[86:87]
	s_addc_u32 s25, s25, 0
	s_add_i32 s26, s29, s1
	global_load_lds_dwordx4 v[182:183], off
	v_lshl_add_u64 v[182:183], s[24:25], 0, v[2:3]
	s_mov_b32 m0, s26
	s_nop 0
	global_load_lds_dwordx4 v[182:183], off
	v_lshl_add_u64 v[182:183], s[24:25], 0, v[168:169]
	s_add_i32 m0, s26, 0x2000
	s_nop 0
	global_load_lds_dwordx4 v[182:183], off
	v_lshl_add_u64 v[182:183], v[240:241], 0, s[86:87]
	s_mov_b32 m0, s78
	s_nop 0
	global_load_lds_dwordx4 v[182:183], off
	v_lshl_add_u64 v[182:183], v[242:243], 0, s[86:87]
	s_mov_b32 m0, s85
	s_nop 0
	global_load_lds_dwordx4 v[182:183], off
	s_waitcnt vmcnt(8)
	s_waitcnt lgkmcnt(0)
	s_barrier
	v_mfma_f32_16x16x32_bf16 v[56:59], v[132:135], v[190:193], v[56:59]
	v_mfma_f32_16x16x32_bf16 v[52:55], v[140:143], v[190:193], v[52:55]
	v_mfma_f32_16x16x32_bf16 v[40:43], v[132:135], v[198:201], v[40:43]
	v_mfma_f32_16x16x32_bf16 v[36:39], v[140:143], v[198:201], v[36:39]
	v_mfma_f32_16x16x32_bf16 v[24:27], v[132:135], v[222:225], v[24:27]
	v_mfma_f32_16x16x32_bf16 v[20:23], v[140:143], v[222:225], v[20:23]
	v_mfma_f32_16x16x32_bf16 v[8:11], v[132:135], v[230:233], v[8:11]
	v_mfma_f32_16x16x32_bf16 v[4:7], v[140:143], v[230:233], v[4:7]
	v_mfma_f32_16x16x32_bf16 v[56:59], v[136:139], v[194:197], v[56:59]
	v_mfma_f32_16x16x32_bf16 v[52:55], v[144:147], v[194:197], v[52:55]
	v_mfma_f32_16x16x32_bf16 v[40:43], v[136:139], v[202:205], v[40:43]
	v_mfma_f32_16x16x32_bf16 v[36:39], v[144:147], v[202:205], v[36:39]
	v_mfma_f32_16x16x32_bf16 v[24:27], v[136:139], v[226:229], v[24:27]
	v_mfma_f32_16x16x32_bf16 v[20:23], v[144:147], v[226:229], v[20:23]
	v_mfma_f32_16x16x32_bf16 v[8:11], v[136:139], v[234:237], v[8:11]
	v_mfma_f32_16x16x32_bf16 v[4:7], v[144:147], v[234:237], v[4:7]
	v_mfma_f32_16x16x32_bf16 v[64:67], v[148:151], v[190:193], v[64:67]
	v_mfma_f32_16x16x32_bf16 v[60:63], v[178:181], v[190:193], v[60:63]
	v_mfma_f32_16x16x32_bf16 v[48:51], v[148:151], v[198:201], v[48:51]
	v_mfma_f32_16x16x32_bf16 v[44:47], v[178:181], v[198:201], v[44:47]
	v_mfma_f32_16x16x32_bf16 v[32:35], v[148:151], v[222:225], v[32:35]
	v_mfma_f32_16x16x32_bf16 v[28:31], v[178:181], v[222:225], v[28:31]
	v_mfma_f32_16x16x32_bf16 v[16:19], v[148:151], v[230:233], v[16:19]
	v_mfma_f32_16x16x32_bf16 v[12:15], v[178:181], v[230:233], v[12:15]
	v_mfma_f32_16x16x32_bf16 v[64:67], v[152:155], v[194:197], v[64:67]
	v_mfma_f32_16x16x32_bf16 v[60:63], v[186:189], v[194:197], v[60:63]
	v_mfma_f32_16x16x32_bf16 v[48:51], v[152:155], v[202:205], v[48:51]
	v_mfma_f32_16x16x32_bf16 v[44:47], v[186:189], v[202:205], v[44:47]
	v_mfma_f32_16x16x32_bf16 v[32:35], v[152:155], v[226:229], v[32:35]
	v_mfma_f32_16x16x32_bf16 v[28:31], v[186:189], v[226:229], v[28:31]
	v_mfma_f32_16x16x32_bf16 v[16:19], v[152:155], v[234:237], v[16:19]
	v_mfma_f32_16x16x32_bf16 v[12:15], v[186:189], v[234:237], v[12:15]
	s_barrier
	s_add_i32 s58, s58, 2
	s_add_u32 s6, s6, 0x100
	s_addc_u32 s7, s7, 0
	s_add_u32 s21, s21, 0x100
	s_addc_u32 s13, s13, 0
	s_cmp_gt_u32 s58, 61
	s_cbranch_scc0 .LBB0_265
	s_setprio 0
	s_and_b64 vcc, exec, s[30:31]
	s_cbranch_vccz .LBB0_268
	s_barrier

.LBB0_721:
	v_bfe_u32 v1, v18, 4, 2
	v_and_b32_e32 v142, 15, v18
	v_lshlrev_b32_e32 v19, 4, v1
	v_lshlrev_b32_e32 v18, 2, v18
	s_and_b32 s44, s21, 3
	v_lshl_or_b32 v19, v142, 6, v19
	s_lshl_b32 s21, s25, 13
	v_and_b32_e32 v18, 32, v18
	s_add_i32 m0, s5, 0x18000
	v_lshl_add_u64 v[10:11], v[10:11], 0, s[86:87]
	s_lshl_b32 s40, s25, 6
	v_bitop3_b32 v20, v19, s21, v18 bitop3:0xde
	s_lshl_b32 s21, s44, 12
	global_load_lds_dwordx4 v[10:11], off
	v_lshl_add_u64 v[8:9], v[8:9], 0, s[86:87]
	s_add_i32 m0, s5, 0x1a000
	s_add_i32 s46, s5, 0x8000
	s_add_i32 s50, s5, 0xa000
	global_load_lds_dwordx4 v[8:9], off
	v_lshl_add_u64 v[6:7], v[6:7], 0, s[86:87]
	s_mov_b32 m0, s46
	s_add_u32 s26, s6, 0x100080
	global_load_lds_dwordx4 v[6:7], off
	v_lshl_add_u64 v[4:5], v[4:5], 0, s[86:87]
	s_mov_b32 m0, s50
	s_addc_u32 s27, s7, 0
	global_load_lds_dwordx4 v[4:5], off
	s_add_i32 m0, s5, 0x1c000
	v_lshl_add_u64 v[4:5], s[26:27], 0, v[2:3]
	global_load_lds_dwordx4 v[4:5], off
	v_lshl_add_u64 v[4:5], s[26:27], 0, v[136:137]
	s_add_i32 m0, s5, 0x1e000
	v_bitop3_b32 v143, v19, s21, v18 bitop3:0xde
	global_load_lds_dwordx4 v[4:5], off
	s_waitcnt vmcnt(8)
	s_barrier
	s_add_u32 s21, s24, s30
	s_addc_u32 s25, 0, s13
	v_lshlrev_b32_e32 v4, 16, v12
	s_add_u32 s51, s36, s21
	v_and_b32_e32 v4, 0xfffe0000, v4
	s_addc_u32 s52, s37, s25
	v_lshl_add_u32 v4, v13, 13, v4
	v_and_b32_e32 v5, 1, v12
	v_readlane_b32 s24, v254, 40
	v_lshl_or_b32 v4, v5, 6, v4
	s_add_u32 s24, s24, s21
	v_readlane_b32 s21, v254, 41
	v_lshl_add_u32 v4, v14, 1, v4
	v_mov_b32_e32 v5, v3
	s_addc_u32 s25, s21, s25
	v_lshl_add_u64 v[138:139], s[24:25], 0, v[4:5]
	v_lshlrev_b32_e32 v4, 16, v15
	v_and_b32_e32 v4, 0xfffe0000, v4
	v_lshl_add_u32 v4, v16, 13, v4
	v_and_b32_e32 v5, 1, v15
	v_lshl_or_b32 v4, v5, 6, v4
	s_add_u32 s10, s10, s30
	s_waitcnt vmcnt(6)
	v_lshl_add_u32 v4, v17, 1, v4
	v_mov_b32_e32 v5, v3
	s_addc_u32 s11, s11, s13
	v_readlane_b32 s13, v254, 42
	v_lshl_add_u64 v[140:141], s[24:25], 0, v[4:5]
	s_add_u32 s13, s13, s10
	v_readlane_b32 s10, v254, 43
	v_mov_b32_e32 v4, 0
	s_addc_u32 s21, s10, s11
	s_mov_b32 s53, -2
	s_mov_b64 s[10:11], 0
	v_add_u32_e32 v144, 0, v20
	v_mov_b32_e32 v5, v4
	v_mov_b32_e32 v6, v4
	v_mov_b32_e32 v7, v4
	v_mov_b32_e32 v8, v4
	v_mov_b32_e32 v9, v4
	v_mov_b32_e32 v10, v4
	v_mov_b32_e32 v11, v4
	v_mov_b32_e32 v16, v4
	v_mov_b32_e32 v17, v4
	v_mov_b32_e32 v18, v4
	v_mov_b32_e32 v19, v4
	v_mov_b32_e32 v24, v4
	v_mov_b32_e32 v25, v4
	v_mov_b32_e32 v26, v4
	v_mov_b32_e32 v27, v4
	v_mov_b32_e32 v32, v4
	v_mov_b32_e32 v33, v4
	v_mov_b32_e32 v34, v4
	v_mov_b32_e32 v35, v4
	v_mov_b32_e32 v40, v4
	v_mov_b32_e32 v41, v4
	v_mov_b32_e32 v42, v4
	v_mov_b32_e32 v43, v4
	v_mov_b32_e32 v48, v4
	v_mov_b32_e32 v49, v4
	v_mov_b32_e32 v50, v4
	v_mov_b32_e32 v51, v4
	v_mov_b32_e32 v56, v4
	v_mov_b32_e32 v57, v4
	v_mov_b32_e32 v58, v4
	v_mov_b32_e32 v59, v4
	v_mov_b32_e32 v12, v4
	v_mov_b32_e32 v13, v4
	v_mov_b32_e32 v14, v4
	v_mov_b32_e32 v15, v4
	v_mov_b32_e32 v20, v4
	v_mov_b32_e32 v21, v4
	v_mov_b32_e32 v22, v4
	v_mov_b32_e32 v23, v4
	v_mov_b32_e32 v28, v4
	v_mov_b32_e32 v29, v4
	v_mov_b32_e32 v30, v4
	v_mov_b32_e32 v31, v4
	v_mov_b32_e32 v36, v4
	v_mov_b32_e32 v37, v4
	v_mov_b32_e32 v38, v4
	v_mov_b32_e32 v39, v4
	v_mov_b32_e32 v44, v4
	v_mov_b32_e32 v45, v4
	v_mov_b32_e32 v46, v4
	v_mov_b32_e32 v47, v4
	v_mov_b32_e32 v52, v4
	v_mov_b32_e32 v53, v4
	v_mov_b32_e32 v54, v4
	v_mov_b32_e32 v55, v4
	v_mov_b32_e32 v60, v4
	v_mov_b32_e32 v61, v4
	v_mov_b32_e32 v62, v4
	v_mov_b32_e32 v63, v4
	v_mov_b32_e32 v64, v4
	v_mov_b32_e32 v65, v4
	v_mov_b32_e32 v66, v4
	v_mov_b32_e32 v67, v4
	v_mov_b32_e32 v68, v4
	v_mov_b32_e32 v69, v4
	v_mov_b32_e32 v70, v4
	v_mov_b32_e32 v71, v4
	v_mov_b32_e32 v72, v4
	v_mov_b32_e32 v73, v4
	v_mov_b32_e32 v74, v4
	v_mov_b32_e32 v75, v4
	v_mov_b32_e32 v80, v4
	v_mov_b32_e32 v81, v4
	v_mov_b32_e32 v82, v4
	v_mov_b32_e32 v83, v4
	v_mov_b32_e32 v88, v4
	v_mov_b32_e32 v89, v4
	v_mov_b32_e32 v90, v4
	v_mov_b32_e32 v91, v4
	v_mov_b32_e32 v96, v4
	v_mov_b32_e32 v97, v4
	v_mov_b32_e32 v98, v4
	v_mov_b32_e32 v99, v4
	v_mov_b32_e32 v104, v4
	v_mov_b32_e32 v105, v4
	v_mov_b32_e32 v106, v4
	v_mov_b32_e32 v107, v4
	v_mov_b32_e32 v112, v4
	v_mov_b32_e32 v113, v4
	v_mov_b32_e32 v114, v4
	v_mov_b32_e32 v115, v4
	v_mov_b32_e32 v120, v4
	v_mov_b32_e32 v121, v4
	v_mov_b32_e32 v122, v4
	v_mov_b32_e32 v123, v4
	v_mov_b32_e32 v76, v4
	v_mov_b32_e32 v77, v4
	v_mov_b32_e32 v78, v4
	v_mov_b32_e32 v79, v4
	v_mov_b32_e32 v84, v4
	v_mov_b32_e32 v85, v4
	v_mov_b32_e32 v86, v4
	v_mov_b32_e32 v87, v4
	v_mov_b32_e32 v92, v4
	v_mov_b32_e32 v93, v4
	v_mov_b32_e32 v94, v4
	v_mov_b32_e32 v95, v4
	v_mov_b32_e32 v100, v4
	v_mov_b32_e32 v101, v4
	v_mov_b32_e32 v102, v4
	v_mov_b32_e32 v103, v4
	v_mov_b32_e32 v108, v4
	v_mov_b32_e32 v109, v4
	v_mov_b32_e32 v110, v4
	v_mov_b32_e32 v111, v4
	v_mov_b32_e32 v116, v4
	v_mov_b32_e32 v117, v4
	v_mov_b32_e32 v118, v4
	v_mov_b32_e32 v119, v4
	v_mov_b32_e32 v124, v4
	v_mov_b32_e32 v125, v4
	v_mov_b32_e32 v126, v4
	v_mov_b32_e32 v127, v4
	v_mov_b32_e32 v128, v4
	v_mov_b32_e32 v129, v4
	v_mov_b32_e32 v130, v4
	v_mov_b32_e32 v131, v4
	s_barrier
	s_cmpk_lt_u32 s23, 0x100
	s_cbranch_scc1 .Lsprio_sa
	s_setprio 1
.Lsprio_sa:
.LBB0_722:
	s_add_u32 s24, s51, s10
	s_addc_u32 s25, s52, s11
	s_add_u32 s24, s24, 0x2b800100
	s_addc_u32 s25, s25, 0
	s_add_u32 s28, s13, s10
	s_addc_u32 s29, s21, s11
	s_add_i32 s54, 0, 0x10000
	s_cmpk_eq_i32 s10, 0x1f00
	s_cselect_b32 s27, s9, s25
	s_cselect_b32 s26, s8, s24
	v_add_u32_e32 v145, s54, v143
	s_cselect_b32 s25, s7, s29
	s_cselect_b32 s24, s6, s28
	s_add_i32 s55, 0, 0x14000
	ds_read_b128 v[146:149], v145
	ds_read_b128 v[150:153], v145 offset:1024
	ds_read_b128 v[170:173], v145 offset:2048
	ds_read_b128 v[174:177], v145 offset:3072
	v_add_u32_e32 v145, s55, v143
	ds_read_b128 v[178:181], v145
	ds_read_b128 v[182:185], v145 offset:1024
	ds_read_b128 v[186:189], v145 offset:2048
	ds_read_b128 v[190:193], v145 offset:3072
	v_lshl_add_u64 v[154:155], v[138:139], 0, s[10:11]
	s_add_i32 m0, s5, 0xc000
	ds_read_b128 v[194:197], v144
	ds_read_b128 v[198:201], v144 offset:1024
	ds_read_b128 v[202:205], v144 offset:2048
	ds_read_b128 v[222:225], v144 offset:3072
	ds_read_b128 v[226:229], v144 offset:4096
	ds_read_b128 v[230:233], v144 offset:5120
	ds_read_b128 v[234:237], v144 offset:6144
	ds_read_b128 v[238:241], v144 offset:7168
	global_load_lds_dwordx4 v[154:155], off
	v_lshl_add_u64 v[154:155], v[140:141], 0, s[10:11]
	s_add_i32 m0, s5, 0xe000
	s_nop 0
	global_load_lds_dwordx4 v[154:155], off
	s_waitcnt vmcnt(8)
	s_waitcnt lgkmcnt(0)
	s_barrier
	v_mfma_f32_16x16x32_bf16 v[128:131], v[146:149], v[194:197], v[128:131]
	v_mfma_f32_16x16x32_bf16 v[124:127], v[170:173], v[194:197], v[124:127]
	v_mfma_f32_16x16x32_bf16 v[116:119], v[146:149], v[202:205], v[116:119]
	v_mfma_f32_16x16x32_bf16 v[108:111], v[170:173], v[202:205], v[108:111]
	v_mfma_f32_16x16x32_bf16 v[100:103], v[146:149], v[226:229], v[100:103]
	v_mfma_f32_16x16x32_bf16 v[92:95], v[170:173], v[226:229], v[92:95]
	v_mfma_f32_16x16x32_bf16 v[84:87], v[146:149], v[234:237], v[84:87]
	v_mfma_f32_16x16x32_bf16 v[76:79], v[170:173], v[234:237], v[76:79]
	v_mfma_f32_16x16x32_bf16 v[128:131], v[150:153], v[198:201], v[128:131]
	v_mfma_f32_16x16x32_bf16 v[124:127], v[174:177], v[198:201], v[124:127]
	v_mfma_f32_16x16x32_bf16 v[116:119], v[150:153], v[222:225], v[116:119]
	v_mfma_f32_16x16x32_bf16 v[108:111], v[174:177], v[222:225], v[108:111]
	v_mfma_f32_16x16x32_bf16 v[100:103], v[150:153], v[230:233], v[100:103]
	v_mfma_f32_16x16x32_bf16 v[92:95], v[174:177], v[230:233], v[92:95]
	v_mfma_f32_16x16x32_bf16 v[84:87], v[150:153], v[238:241], v[84:87]
	v_mfma_f32_16x16x32_bf16 v[76:79], v[174:177], v[238:241], v[76:79]
	v_mfma_f32_16x16x32_bf16 v[120:123], v[178:181], v[194:197], v[120:123]
	v_mfma_f32_16x16x32_bf16 v[112:115], v[186:189], v[194:197], v[112:115]
	v_mfma_f32_16x16x32_bf16 v[104:107], v[178:181], v[202:205], v[104:107]
	v_mfma_f32_16x16x32_bf16 v[96:99], v[186:189], v[202:205], v[96:99]
	v_mfma_f32_16x16x32_bf16 v[88:91], v[178:181], v[226:229], v[88:91]
	v_mfma_f32_16x16x32_bf16 v[80:83], v[186:189], v[226:229], v[80:83]
	v_mfma_f32_16x16x32_bf16 v[72:75], v[178:181], v[234:237], v[72:75]
	v_mfma_f32_16x16x32_bf16 v[68:71], v[186:189], v[234:237], v[68:71]
	v_mfma_f32_16x16x32_bf16 v[120:123], v[182:185], v[198:201], v[120:123]
	v_mfma_f32_16x16x32_bf16 v[112:115], v[190:193], v[198:201], v[112:115]
	v_mfma_f32_16x16x32_bf16 v[104:107], v[182:185], v[222:225], v[104:107]
	v_mfma_f32_16x16x32_bf16 v[96:99], v[190:193], v[222:225], v[96:99]
	v_mfma_f32_16x16x32_bf16 v[88:91], v[182:185], v[230:233], v[88:91]
	v_mfma_f32_16x16x32_bf16 v[80:83], v[190:193], v[230:233], v[80:83]
	v_mfma_f32_16x16x32_bf16 v[72:75], v[182:185], v[238:241], v[72:75]
	v_mfma_f32_16x16x32_bf16 v[68:71], v[190:193], v[238:241], v[68:71]
	s_barrier
	s_add_i32 s28, s54, s31
	v_lshl_add_u64 v[154:155], s[24:25], 0, v[2:3]
	s_mov_b32 m0, s28
	ds_read_b128 v[194:197], v144 offset:16384
	ds_read_b128 v[198:201], v144 offset:17408
	ds_read_b128 v[202:205], v144 offset:18432
	ds_read_b128 v[222:225], v144 offset:19456
	ds_read_b128 v[226:229], v144 offset:20480
	ds_read_b128 v[230:233], v144 offset:21504
	ds_read_b128 v[234:237], v144 offset:22528
	ds_read_b128 v[238:241], v144 offset:23552
	global_load_lds_dwordx4 v[154:155], off
	s_add_i32 m0, s28, 0x2000
	s_add_u32 s28, s24, 0x100000
	v_lshl_add_u64 v[242:243], s[24:25], 0, v[136:137]
	s_addc_u32 s29, s25, 0
	s_add_i32 s54, s55, s31
	global_load_lds_dwordx4 v[242:243], off
	v_lshl_add_u64 v[244:245], s[28:29], 0, v[2:3]
	s_mov_b32 m0, s54
	v_lshl_add_u64 v[246:247], s[26:27], 0, v[134:135]
	global_load_lds_dwordx4 v[244:245], off
	v_lshl_add_u64 v[244:245], s[28:29], 0, v[136:137]
	s_add_i32 m0, s54, 0x2000
	s_nop 0
	global_load_lds_dwordx4 v[244:245], off
	v_lshl_add_u64 v[244:245], s[26:27], 0, v[132:133]
	s_mov_b32 m0, s5
	s_nop 0
	global_load_lds_dwordx4 v[244:245], off
	s_mov_b32 m0, s35
	s_nop 0
	global_load_lds_dwordx4 v[246:247], off
	s_waitcnt vmcnt(8)
	s_waitcnt lgkmcnt(0)
	s_barrier
	v_mfma_f32_16x16x32_bf16 v[64:67], v[146:149], v[194:197], v[64:67]
	v_mfma_f32_16x16x32_bf16 v[60:63], v[170:173], v[194:197], v[60:63]
	v_mfma_f32_16x16x32_bf16 v[52:55], v[146:149], v[202:205], v[52:55]
	v_mfma_f32_16x16x32_bf16 v[44:47], v[170:173], v[202:205], v[44:47]
	v_mfma_f32_16x16x32_bf16 v[36:39], v[146:149], v[226:229], v[36:39]
	v_mfma_f32_16x16x32_bf16 v[28:31], v[170:173], v[226:229], v[28:31]
	v_mfma_f32_16x16x32_bf16 v[20:23], v[146:149], v[234:237], v[20:23]
	v_mfma_f32_16x16x32_bf16 v[12:15], v[170:173], v[234:237], v[12:15]
	v_mfma_f32_16x16x32_bf16 v[64:67], v[150:153], v[198:201], v[64:67]
	v_mfma_f32_16x16x32_bf16 v[60:63], v[174:177], v[198:201], v[60:63]
	v_mfma_f32_16x16x32_bf16 v[52:55], v[150:153], v[222:225], v[52:55]
	v_mfma_f32_16x16x32_bf16 v[44:47], v[174:177], v[222:225], v[44:47]
	v_mfma_f32_16x16x32_bf16 v[36:39], v[150:153], v[230:233], v[36:39]
	v_mfma_f32_16x16x32_bf16 v[28:31], v[174:177], v[230:233], v[28:31]
	v_mfma_f32_16x16x32_bf16 v[20:23], v[150:153], v[238:241], v[20:23]
	v_mfma_f32_16x16x32_bf16 v[12:15], v[174:177], v[238:241], v[12:15]
	v_mfma_f32_16x16x32_bf16 v[56:59], v[178:181], v[194:197], v[56:59]
	v_mfma_f32_16x16x32_bf16 v[48:51], v[186:189], v[194:197], v[48:51]
	v_mfma_f32_16x16x32_bf16 v[40:43], v[178:181], v[202:205], v[40:43]
	v_mfma_f32_16x16x32_bf16 v[32:35], v[186:189], v[202:205], v[32:35]
	v_mfma_f32_16x16x32_bf16 v[24:27], v[178:181], v[226:229], v[24:27]
	v_mfma_f32_16x16x32_bf16 v[16:19], v[186:189], v[226:229], v[16:19]
	v_mfma_f32_16x16x32_bf16 v[8:11], v[178:181], v[234:237], v[8:11]
	v_mfma_f32_16x16x32_bf16 v[4:7], v[186:189], v[234:237], v[4:7]
	v_mfma_f32_16x16x32_bf16 v[56:59], v[182:185], v[198:201], v[56:59]
	v_mfma_f32_16x16x32_bf16 v[48:51], v[190:193], v[198:201], v[48:51]
	v_mfma_f32_16x16x32_bf16 v[40:43], v[182:185], v[222:225], v[40:43]
	v_mfma_f32_16x16x32_bf16 v[32:35], v[190:193], v[222:225], v[32:35]
	v_mfma_f32_16x16x32_bf16 v[24:27], v[182:185], v[230:233], v[24:27]
	v_mfma_f32_16x16x32_bf16 v[16:19], v[190:193], v[230:233], v[16:19]
	v_mfma_f32_16x16x32_bf16 v[8:11], v[182:185], v[238:241], v[8:11]
	v_mfma_f32_16x16x32_bf16 v[4:7], v[190:193], v[238:241], v[4:7]
	s_barrier
	s_add_i32 s28, 0, 0x18000
	v_add_u32_e32 v145, s28, v143
	s_add_i32 s29, 0, 0x1c000
	ds_read_b128 v[146:149], v145
	ds_read_b128 v[150:153], v145 offset:1024
	ds_read_b128 v[170:173], v145 offset:2048
	ds_read_b128 v[174:177], v145 offset:3072
	v_add_u32_e32 v145, s29, v143
	ds_read_b128 v[178:181], v145
	ds_read_b128 v[182:185], v145 offset:1024
	ds_read_b128 v[186:189], v145 offset:2048
	ds_read_b128 v[190:193], v145 offset:3072
	s_add_u32 s26, s26, 0x100000
	s_addc_u32 s27, s27, 0
	s_mov_b32 m0, s38
	v_lshl_add_u64 v[248:249], s[26:27], 0, v[132:133]
	ds_read_b128 v[194:197], v144 offset:32768
	ds_read_b128 v[198:201], v144 offset:33792
	ds_read_b128 v[202:205], v144 offset:34816
	ds_read_b128 v[222:225], v144 offset:35840
	ds_read_b128 v[226:229], v144 offset:36864
	ds_read_b128 v[230:233], v144 offset:37888
	ds_read_b128 v[234:237], v144 offset:38912
	ds_read_b128 v[238:241], v144 offset:39936
	global_load_lds_dwordx4 v[248:249], off
	v_lshl_add_u64 v[248:249], s[26:27], 0, v[134:135]
	s_mov_b32 m0, s42
	s_nop 0
	global_load_lds_dwordx4 v[248:249], off
	s_waitcnt vmcnt(8)
	s_waitcnt lgkmcnt(0)
	s_barrier
	v_mfma_f32_16x16x32_bf16 v[128:131], v[146:149], v[194:197], v[128:131]
	v_mfma_f32_16x16x32_bf16 v[124:127], v[170:173], v[194:197], v[124:127]
	v_mfma_f32_16x16x32_bf16 v[116:119], v[146:149], v[202:205], v[116:119]
	v_mfma_f32_16x16x32_bf16 v[108:111], v[170:173], v[202:205], v[108:111]
	v_mfma_f32_16x16x32_bf16 v[100:103], v[146:149], v[226:229], v[100:103]
	v_mfma_f32_16x16x32_bf16 v[92:95], v[170:173], v[226:229], v[92:95]
	v_mfma_f32_16x16x32_bf16 v[84:87], v[146:149], v[234:237], v[84:87]
	v_mfma_f32_16x16x32_bf16 v[76:79], v[170:173], v[234:237], v[76:79]
	v_mfma_f32_16x16x32_bf16 v[128:131], v[150:153], v[198:201], v[128:131]
	v_mfma_f32_16x16x32_bf16 v[124:127], v[174:177], v[198:201], v[124:127]
	v_mfma_f32_16x16x32_bf16 v[116:119], v[150:153], v[222:225], v[116:119]
	v_mfma_f32_16x16x32_bf16 v[108:111], v[174:177], v[222:225], v[108:111]
	v_mfma_f32_16x16x32_bf16 v[100:103], v[150:153], v[230:233], v[100:103]
	v_mfma_f32_16x16x32_bf16 v[92:95], v[174:177], v[230:233], v[92:95]
	v_mfma_f32_16x16x32_bf16 v[84:87], v[150:153], v[238:241], v[84:87]
	v_mfma_f32_16x16x32_bf16 v[76:79], v[174:177], v[238:241], v[76:79]
	v_mfma_f32_16x16x32_bf16 v[120:123], v[178:181], v[194:197], v[120:123]
	v_mfma_f32_16x16x32_bf16 v[112:115], v[186:189], v[194:197], v[112:115]
	v_mfma_f32_16x16x32_bf16 v[104:107], v[178:181], v[202:205], v[104:107]
	v_mfma_f32_16x16x32_bf16 v[96:99], v[186:189], v[202:205], v[96:99]
	v_mfma_f32_16x16x32_bf16 v[88:91], v[178:181], v[226:229], v[88:91]
	v_mfma_f32_16x16x32_bf16 v[80:83], v[186:189], v[226:229], v[80:83]
	v_mfma_f32_16x16x32_bf16 v[72:75], v[178:181], v[234:237], v[72:75]
	v_mfma_f32_16x16x32_bf16 v[68:71], v[186:189], v[234:237], v[68:71]
	v_mfma_f32_16x16x32_bf16 v[120:123], v[182:185], v[198:201], v[120:123]
	v_mfma_f32_16x16x32_bf16 v[112:115], v[190:193], v[198:201], v[112:115]
	v_mfma_f32_16x16x32_bf16 v[104:107], v[182:185], v[222:225], v[104:107]
	v_mfma_f32_16x16x32_bf16 v[96:99], v[190:193], v[222:225], v[96:99]
	v_mfma_f32_16x16x32_bf16 v[88:91], v[182:185], v[230:233], v[88:91]
	v_mfma_f32_16x16x32_bf16 v[80:83], v[190:193], v[230:233], v[80:83]
	v_mfma_f32_16x16x32_bf16 v[72:75], v[182:185], v[238:241], v[72:75]
	v_mfma_f32_16x16x32_bf16 v[68:71], v[190:193], v[238:241], v[68:71]
	s_barrier
	s_add_i32 s26, s28, s31
	v_lshl_add_u64 v[154:155], v[154:155], 0, s[86:87]
	s_mov_b32 m0, s26
	ds_read_b128 v[194:197], v144 offset:49152
	ds_read_b128 v[198:201], v144 offset:50176
	ds_read_b128 v[202:205], v144 offset:51200
	ds_read_b128 v[222:225], v144 offset:52224
	ds_read_b128 v[226:229], v144 offset:53248
	ds_read_b128 v[230:233], v144 offset:54272
	ds_read_b128 v[234:237], v144 offset:55296
	ds_read_b128 v[238:241], v144 offset:56320
	global_load_lds_dwordx4 v[154:155], off
	s_add_i32 m0, s26, 0x2000
	s_add_u32 s24, s24, 0x100080
	v_lshl_add_u64 v[154:155], v[242:243], 0, s[86:87]
	s_addc_u32 s25, s25, 0
	s_add_i32 s26, s29, s31
	global_load_lds_dwordx4 v[154:155], off
	v_lshl_add_u64 v[154:155], s[24:25], 0, v[2:3]
	s_mov_b32 m0, s26
	s_nop 0
	global_load_lds_dwordx4 v[154:155], off
	v_lshl_add_u64 v[154:155], s[24:25], 0, v[136:137]
	s_add_i32 m0, s26, 0x2000
	s_nop 0
	global_load_lds_dwordx4 v[154:155], off
	v_lshl_add_u64 v[154:155], v[244:245], 0, s[86:87]
	s_mov_b32 m0, s46
	s_nop 0
	global_load_lds_dwordx4 v[154:155], off
	v_lshl_add_u64 v[154:155], v[246:247], 0, s[86:87]
	s_mov_b32 m0, s50
	s_nop 0
	global_load_lds_dwordx4 v[154:155], off
	s_waitcnt vmcnt(8)
	s_waitcnt lgkmcnt(0)
	s_barrier
	v_mfma_f32_16x16x32_bf16 v[64:67], v[146:149], v[194:197], v[64:67]
	v_mfma_f32_16x16x32_bf16 v[60:63], v[170:173], v[194:197], v[60:63]
	v_mfma_f32_16x16x32_bf16 v[52:55], v[146:149], v[202:205], v[52:55]
	v_mfma_f32_16x16x32_bf16 v[44:47], v[170:173], v[202:205], v[44:47]
	v_mfma_f32_16x16x32_bf16 v[36:39], v[146:149], v[226:229], v[36:39]
	v_mfma_f32_16x16x32_bf16 v[28:31], v[170:173], v[226:229], v[28:31]
	v_mfma_f32_16x16x32_bf16 v[20:23], v[146:149], v[234:237], v[20:23]
	v_mfma_f32_16x16x32_bf16 v[12:15], v[170:173], v[234:237], v[12:15]
	v_mfma_f32_16x16x32_bf16 v[64:67], v[150:153], v[198:201], v[64:67]
	v_mfma_f32_16x16x32_bf16 v[60:63], v[174:177], v[198:201], v[60:63]
	v_mfma_f32_16x16x32_bf16 v[52:55], v[150:153], v[222:225], v[52:55]
	v_mfma_f32_16x16x32_bf16 v[44:47], v[174:177], v[222:225], v[44:47]
	v_mfma_f32_16x16x32_bf16 v[36:39], v[150:153], v[230:233], v[36:39]
	v_mfma_f32_16x16x32_bf16 v[28:31], v[174:177], v[230:233], v[28:31]
	v_mfma_f32_16x16x32_bf16 v[20:23], v[150:153], v[238:241], v[20:23]
	v_mfma_f32_16x16x32_bf16 v[12:15], v[174:177], v[238:241], v[12:15]
	v_mfma_f32_16x16x32_bf16 v[56:59], v[178:181], v[194:197], v[56:59]
	v_mfma_f32_16x16x32_bf16 v[48:51], v[186:189], v[194:197], v[48:51]
	v_mfma_f32_16x16x32_bf16 v[40:43], v[178:181], v[202:205], v[40:43]
	v_mfma_f32_16x16x32_bf16 v[32:35], v[186:189], v[202:205], v[32:35]
	v_mfma_f32_16x16x32_bf16 v[24:27], v[178:181], v[226:229], v[24:27]
	v_mfma_f32_16x16x32_bf16 v[16:19], v[186:189], v[226:229], v[16:19]
	v_mfma_f32_16x16x32_bf16 v[8:11], v[178:181], v[234:237], v[8:11]
	v_mfma_f32_16x16x32_bf16 v[4:7], v[186:189], v[234:237], v[4:7]
	v_mfma_f32_16x16x32_bf16 v[56:59], v[182:185], v[198:201], v[56:59]
	v_mfma_f32_16x16x32_bf16 v[48:51], v[190:193], v[198:201], v[48:51]
	v_mfma_f32_16x16x32_bf16 v[40:43], v[182:185], v[222:225], v[40:43]
	v_mfma_f32_16x16x32_bf16 v[32:35], v[190:193], v[222:225], v[32:35]
	v_mfma_f32_16x16x32_bf16 v[24:27], v[182:185], v[230:233], v[24:27]
	v_mfma_f32_16x16x32_bf16 v[16:19], v[190:193], v[230:233], v[16:19]
	v_mfma_f32_16x16x32_bf16 v[8:11], v[182:185], v[238:241], v[8:11]
	v_mfma_f32_16x16x32_bf16 v[4:7], v[190:193], v[238:241], v[4:7]
	s_barrier
	s_add_i32 s53, s53, 2
	s_add_u32 s10, s10, 0x100
	s_addc_u32 s11, s11, 0
	s_cmp_gt_u32 s53, 61
	s_cbranch_scc0 .LBB0_722
	s_setprio 0
	s_cmpk_lt_u32 s23, 0x100
	s_cbranch_scc0 .LBB0_725
	s_barrier

.LBB0_1201:
	s_ashr_i32 s53, s52, 31
	s_lshl_b64 s[26:27], s[52:53], 21
	s_add_u32 s72, s38, s26
	s_addc_u32 s73, s40, s27
	s_and_b64 s[26:27], s[4:5], exec
	s_cselect_b32 s35, s73, s7
	s_cselect_b32 s53, s72, s6
	s_ashr_i32 s31, s30, 31
	s_lshl_b64 s[26:27], s[30:31], 21
	s_add_u32 s74, s42, s26
	s_addc_u32 s75, s44, s27
	s_and_b64 s[26:27], s[4:5], exec
	s_cselect_b32 s31, s75, s25
	s_cselect_b32 s92, s74, s24
	s_add_u32 s6, s6, 0x100080
	s_addc_u32 s7, s7, 0
	s_add_u32 s21, s24, 0x100
	s_addc_u32 s13, s25, 0
	s_mov_b32 s58, -2
	s_waitcnt lgkmcnt(0)
	s_cmp_eq_u64 s[14:15], 0
	s_cbranch_scc0 .Lsprio_op
	s_setprio 1
.Lsprio_op:
	s_add_u32 s24, s6, 0xfff00080
	s_addc_u32 s25, s7, -1
	s_add_i32 s28, 0, 0x10000
	s_cmp_eq_u32 s58, 60
	s_cselect_b32 s27, s35, s25
	s_cselect_b32 s26, s53, s24
	s_cselect_b32 s25, s31, s13
	s_cselect_b32 s24, s92, s21
	s_add_i32 s71, 0, 0x14000
	v_add_u32_e32 v150, s28, v163
	v_add_u32_e32 v154, s71, v163
	ds_read_b128 v[138:141], v150
	ds_read_b128 v[142:145], v150 offset:1024
	ds_read_b128 v[146:149], v150 offset:2048
	ds_read_b128 v[150:153], v150 offset:3072
	ds_read_b128 v[168:171], v154
	ds_read_b128 v[172:175], v154 offset:1024
	ds_read_b128 v[176:179], v154 offset:2048
	ds_read_b128 v[180:183], v154 offset:3072
	v_lshl_add_u64 v[154:155], s[6:7], 0, v[134:135]
	s_add_i32 m0, s50, 0xc000
	ds_read_b128 v[188:191], v186
	ds_read_b128 v[192:195], v186 offset:1024
	ds_read_b128 v[196:199], v186 offset:2048
	ds_read_b128 v[200:203], v186 offset:3072
	ds_read_b128 v[222:225], v186 offset:4096
	ds_read_b128 v[226:229], v186 offset:5120
	ds_read_b128 v[230:233], v186 offset:6144
	ds_read_b128 v[234:237], v186 offset:7168
	global_load_lds_dwordx4 v[154:155], off
	v_lshl_add_u64 v[154:155], s[6:7], 0, v[136:137]
	s_add_i32 m0, s50, 0xe000
	s_nop 0
	global_load_lds_dwordx4 v[154:155], off
	s_waitcnt vmcnt(8)
	s_waitcnt lgkmcnt(0)
	s_barrier
	v_mfma_f32_16x16x32_bf16 v[128:131], v[138:141], v[188:191], 0
	v_mfma_f32_16x16x32_bf16 v[124:127], v[146:149], v[188:191], 0
	v_mfma_f32_16x16x32_bf16 v[112:115], v[138:141], v[196:199], 0
	v_mfma_f32_16x16x32_bf16 v[108:111], v[146:149], v[196:199], 0
	v_mfma_f32_16x16x32_bf16 v[96:99], v[138:141], v[222:225], 0
	v_mfma_f32_16x16x32_bf16 v[92:95], v[146:149], v[222:225], 0
	v_mfma_f32_16x16x32_bf16 v[80:83], v[138:141], v[230:233], 0
	v_mfma_f32_16x16x32_bf16 v[76:79], v[146:149], v[230:233], 0
	v_mfma_f32_16x16x32_bf16 v[128:131], v[142:145], v[192:195], v[128:131]
	v_mfma_f32_16x16x32_bf16 v[124:127], v[150:153], v[192:195], v[124:127]
	v_mfma_f32_16x16x32_bf16 v[112:115], v[142:145], v[200:203], v[112:115]
	v_mfma_f32_16x16x32_bf16 v[108:111], v[150:153], v[200:203], v[108:111]
	v_mfma_f32_16x16x32_bf16 v[96:99], v[142:145], v[226:229], v[96:99]
	v_mfma_f32_16x16x32_bf16 v[92:95], v[150:153], v[226:229], v[92:95]
	v_mfma_f32_16x16x32_bf16 v[80:83], v[142:145], v[234:237], v[80:83]
	v_mfma_f32_16x16x32_bf16 v[76:79], v[150:153], v[234:237], v[76:79]
	v_mfma_f32_16x16x32_bf16 v[120:123], v[168:171], v[188:191], 0
	v_mfma_f32_16x16x32_bf16 v[116:119], v[176:179], v[188:191], 0
	v_mfma_f32_16x16x32_bf16 v[104:107], v[168:171], v[196:199], 0
	v_mfma_f32_16x16x32_bf16 v[100:103], v[176:179], v[196:199], 0
	v_mfma_f32_16x16x32_bf16 v[88:91], v[168:171], v[222:225], 0
	v_mfma_f32_16x16x32_bf16 v[84:87], v[176:179], v[222:225], 0
	v_mfma_f32_16x16x32_bf16 v[72:75], v[168:171], v[230:233], 0
	v_mfma_f32_16x16x32_bf16 v[68:71], v[176:179], v[230:233], 0
	v_mfma_f32_16x16x32_bf16 v[120:123], v[172:175], v[192:195], v[120:123]
	v_mfma_f32_16x16x32_bf16 v[116:119], v[180:183], v[192:195], v[116:119]
	v_mfma_f32_16x16x32_bf16 v[104:107], v[172:175], v[200:203], v[104:107]
	v_mfma_f32_16x16x32_bf16 v[100:103], v[180:183], v[200:203], v[100:103]
	v_mfma_f32_16x16x32_bf16 v[88:91], v[172:175], v[226:229], v[88:91]
	v_mfma_f32_16x16x32_bf16 v[84:87], v[180:183], v[226:229], v[84:87]
	v_mfma_f32_16x16x32_bf16 v[72:75], v[172:175], v[234:237], v[72:75]
	v_mfma_f32_16x16x32_bf16 v[68:71], v[180:183], v[234:237], v[68:71]
	s_barrier
	s_add_i32 s28, s28, s46
	v_lshl_add_u64 v[154:155], s[24:25], 0, v[2:3]
	s_mov_b32 m0, s28
	ds_read_b128 v[188:191], v186 offset:16384
	ds_read_b128 v[192:195], v186 offset:17408
	ds_read_b128 v[196:199], v186 offset:18432
	ds_read_b128 v[200:203], v186 offset:19456
	ds_read_b128 v[222:225], v186 offset:20480
	ds_read_b128 v[226:229], v186 offset:21504
	ds_read_b128 v[230:233], v186 offset:22528
	ds_read_b128 v[234:237], v186 offset:23552
	global_load_lds_dwordx4 v[154:155], off
	s_add_i32 m0, s28, 0x2000
	s_add_u32 s28, s24, 0x100000
	v_lshl_add_u64 v[184:185], s[24:25], 0, v[132:133]
	s_addc_u32 s29, s25, 0
	s_add_i32 s71, s71, s46
	global_load_lds_dwordx4 v[184:185], off
	v_lshl_add_u64 v[204:205], s[28:29], 0, v[2:3]
	s_mov_b32 m0, s71
	v_lshl_add_u64 v[238:239], s[26:27], 0, v[132:133]
	global_load_lds_dwordx4 v[204:205], off
	v_lshl_add_u64 v[204:205], s[28:29], 0, v[132:133]
	s_add_i32 m0, s71, 0x2000
	s_nop 0
	global_load_lds_dwordx4 v[204:205], off
	v_lshl_add_u64 v[204:205], s[26:27], 0, v[2:3]
	s_mov_b32 m0, s50
	s_nop 0
	global_load_lds_dwordx4 v[204:205], off
	s_mov_b32 m0, s23
	s_nop 0
	global_load_lds_dwordx4 v[238:239], off
	s_waitcnt vmcnt(8)
	s_waitcnt lgkmcnt(0)
	s_barrier
	v_mfma_f32_16x16x32_bf16 v[64:67], v[138:141], v[188:191], 0
	v_mfma_f32_16x16x32_bf16 v[60:63], v[146:149], v[188:191], 0
	v_mfma_f32_16x16x32_bf16 v[48:51], v[138:141], v[196:199], 0
	v_mfma_f32_16x16x32_bf16 v[44:47], v[146:149], v[196:199], 0
	v_mfma_f32_16x16x32_bf16 v[32:35], v[138:141], v[222:225], 0
	v_mfma_f32_16x16x32_bf16 v[28:31], v[146:149], v[222:225], 0
	v_mfma_f32_16x16x32_bf16 v[16:19], v[138:141], v[230:233], 0
	v_mfma_f32_16x16x32_bf16 v[12:15], v[146:149], v[230:233], 0
	v_mfma_f32_16x16x32_bf16 v[64:67], v[142:145], v[192:195], v[64:67]
	v_mfma_f32_16x16x32_bf16 v[60:63], v[150:153], v[192:195], v[60:63]
	v_mfma_f32_16x16x32_bf16 v[48:51], v[142:145], v[200:203], v[48:51]
	v_mfma_f32_16x16x32_bf16 v[44:47], v[150:153], v[200:203], v[44:47]
	v_mfma_f32_16x16x32_bf16 v[32:35], v[142:145], v[226:229], v[32:35]
	v_mfma_f32_16x16x32_bf16 v[28:31], v[150:153], v[226:229], v[28:31]
	v_mfma_f32_16x16x32_bf16 v[16:19], v[142:145], v[234:237], v[16:19]
	v_mfma_f32_16x16x32_bf16 v[12:15], v[150:153], v[234:237], v[12:15]
	v_mfma_f32_16x16x32_bf16 v[56:59], v[168:171], v[188:191], 0
	v_mfma_f32_16x16x32_bf16 v[52:55], v[176:179], v[188:191], 0
	v_mfma_f32_16x16x32_bf16 v[40:43], v[168:171], v[196:199], 0
	v_mfma_f32_16x16x32_bf16 v[36:39], v[176:179], v[196:199], 0
	v_mfma_f32_16x16x32_bf16 v[24:27], v[168:171], v[222:225], 0
	v_mfma_f32_16x16x32_bf16 v[20:23], v[176:179], v[222:225], 0
	v_mfma_f32_16x16x32_bf16 v[8:11], v[168:171], v[230:233], 0
	v_mfma_f32_16x16x32_bf16 v[4:7], v[176:179], v[230:233], 0
	v_mfma_f32_16x16x32_bf16 v[56:59], v[172:175], v[192:195], v[56:59]
	v_mfma_f32_16x16x32_bf16 v[52:55], v[180:183], v[192:195], v[52:55]
	v_mfma_f32_16x16x32_bf16 v[40:43], v[172:175], v[200:203], v[40:43]
	v_mfma_f32_16x16x32_bf16 v[36:39], v[180:183], v[200:203], v[36:39]
	v_mfma_f32_16x16x32_bf16 v[24:27], v[172:175], v[226:229], v[24:27]
	v_mfma_f32_16x16x32_bf16 v[20:23], v[180:183], v[226:229], v[20:23]
	v_mfma_f32_16x16x32_bf16 v[8:11], v[172:175], v[234:237], v[8:11]
	v_mfma_f32_16x16x32_bf16 v[4:7], v[180:183], v[234:237], v[4:7]
	s_barrier
	s_add_i32 s28, 0, 0x18000
	s_add_i32 s29, 0, 0x1c000
	v_add_u32_e32 v150, s28, v163
	v_add_u32_e32 v180, s29, v163
	ds_read_b128 v[138:141], v150
	ds_read_b128 v[142:145], v150 offset:1024
	ds_read_b128 v[146:149], v150 offset:2048
	ds_read_b128 v[150:153], v150 offset:3072
	ds_read_b128 v[168:171], v180
	ds_read_b128 v[172:175], v180 offset:1024
	ds_read_b128 v[176:179], v180 offset:2048
	ds_read_b128 v[180:183], v180 offset:3072
	s_add_u32 s26, s26, 0x100000
	s_addc_u32 s27, s27, 0
	s_mov_b32 m0, s51
	v_lshl_add_u64 v[240:241], s[26:27], 0, v[2:3]
	ds_read_b128 v[188:191], v186 offset:32768
	ds_read_b128 v[192:195], v186 offset:33792
	ds_read_b128 v[196:199], v186 offset:34816
	ds_read_b128 v[200:203], v186 offset:35840
	ds_read_b128 v[222:225], v186 offset:36864
	ds_read_b128 v[226:229], v186 offset:37888
	ds_read_b128 v[230:233], v186 offset:38912
	ds_read_b128 v[234:237], v186 offset:39936
	global_load_lds_dwordx4 v[240:241], off
	v_lshl_add_u64 v[240:241], s[26:27], 0, v[132:133]
	s_mov_b32 m0, s54
	s_nop 0
	global_load_lds_dwordx4 v[240:241], off
	s_waitcnt vmcnt(8)
	s_waitcnt lgkmcnt(0)
	s_barrier
	v_mfma_f32_16x16x32_bf16 v[128:131], v[138:141], v[188:191], v[128:131]
	v_mfma_f32_16x16x32_bf16 v[124:127], v[146:149], v[188:191], v[124:127]
	v_mfma_f32_16x16x32_bf16 v[112:115], v[138:141], v[196:199], v[112:115]
	v_mfma_f32_16x16x32_bf16 v[108:111], v[146:149], v[196:199], v[108:111]
	v_mfma_f32_16x16x32_bf16 v[96:99], v[138:141], v[222:225], v[96:99]
	v_mfma_f32_16x16x32_bf16 v[92:95], v[146:149], v[222:225], v[92:95]
	v_mfma_f32_16x16x32_bf16 v[80:83], v[138:141], v[230:233], v[80:83]
	v_mfma_f32_16x16x32_bf16 v[76:79], v[146:149], v[230:233], v[76:79]
	v_mfma_f32_16x16x32_bf16 v[128:131], v[142:145], v[192:195], v[128:131]
	v_mfma_f32_16x16x32_bf16 v[124:127], v[150:153], v[192:195], v[124:127]
	v_mfma_f32_16x16x32_bf16 v[112:115], v[142:145], v[200:203], v[112:115]
	v_mfma_f32_16x16x32_bf16 v[108:111], v[150:153], v[200:203], v[108:111]
	v_mfma_f32_16x16x32_bf16 v[96:99], v[142:145], v[226:229], v[96:99]
	v_mfma_f32_16x16x32_bf16 v[92:95], v[150:153], v[226:229], v[92:95]
	v_mfma_f32_16x16x32_bf16 v[80:83], v[142:145], v[234:237], v[80:83]
	v_mfma_f32_16x16x32_bf16 v[76:79], v[150:153], v[234:237], v[76:79]
	v_mfma_f32_16x16x32_bf16 v[120:123], v[168:171], v[188:191], v[120:123]
	v_mfma_f32_16x16x32_bf16 v[116:119], v[176:179], v[188:191], v[116:119]
	v_mfma_f32_16x16x32_bf16 v[104:107], v[168:171], v[196:199], v[104:107]
	v_mfma_f32_16x16x32_bf16 v[100:103], v[176:179], v[196:199], v[100:103]
	v_mfma_f32_16x16x32_bf16 v[88:91], v[168:171], v[222:225], v[88:91]
	v_mfma_f32_16x16x32_bf16 v[84:87], v[176:179], v[222:225], v[84:87]
	v_mfma_f32_16x16x32_bf16 v[72:75], v[168:171], v[230:233], v[72:75]
	v_mfma_f32_16x16x32_bf16 v[68:71], v[176:179], v[230:233], v[68:71]
	v_mfma_f32_16x16x32_bf16 v[120:123], v[172:175], v[192:195], v[120:123]
	v_mfma_f32_16x16x32_bf16 v[116:119], v[180:183], v[192:195], v[116:119]
	v_mfma_f32_16x16x32_bf16 v[104:107], v[172:175], v[200:203], v[104:107]
	v_mfma_f32_16x16x32_bf16 v[100:103], v[180:183], v[200:203], v[100:103]
	v_mfma_f32_16x16x32_bf16 v[88:91], v[172:175], v[226:229], v[88:91]
	v_mfma_f32_16x16x32_bf16 v[84:87], v[180:183], v[226:229], v[84:87]
	v_mfma_f32_16x16x32_bf16 v[72:75], v[172:175], v[234:237], v[72:75]
	v_mfma_f32_16x16x32_bf16 v[68:71], v[180:183], v[234:237], v[68:71]
	s_barrier
	s_add_i32 s26, s28, s46
	v_lshl_add_u64 v[154:155], v[154:155], 0, s[86:87]
	s_mov_b32 m0, s26
	ds_read_b128 v[188:191], v186 offset:49152
	ds_read_b128 v[192:195], v186 offset:50176
	ds_read_b128 v[196:199], v186 offset:51200
	ds_read_b128 v[200:203], v186 offset:52224
	ds_read_b128 v[222:225], v186 offset:53248
	ds_read_b128 v[226:229], v186 offset:54272
	ds_read_b128 v[230:233], v186 offset:55296
	ds_read_b128 v[234:237], v186 offset:56320
	global_load_lds_dwordx4 v[154:155], off
	s_add_i32 m0, s26, 0x2000
	s_add_u32 s24, s24, 0x100080
	v_lshl_add_u64 v[154:155], v[184:185], 0, s[86:87]
	s_addc_u32 s25, s25, 0
	s_add_i32 s26, s29, s46
	global_load_lds_dwordx4 v[154:155], off
	v_lshl_add_u64 v[154:155], s[24:25], 0, v[2:3]
	s_mov_b32 m0, s26
	s_nop 0
	global_load_lds_dwordx4 v[154:155], off
	v_lshl_add_u64 v[154:155], s[24:25], 0, v[132:133]
	s_add_i32 m0, s26, 0x2000
	s_nop 0
	global_load_lds_dwordx4 v[154:155], off
	v_lshl_add_u64 v[154:155], v[204:205], 0, s[86:87]
	s_mov_b32 m0, s76
	s_nop 0
	global_load_lds_dwordx4 v[154:155], off
	v_lshl_add_u64 v[154:155], v[238:239], 0, s[86:87]
	s_mov_b32 m0, s77
	s_nop 0
	global_load_lds_dwordx4 v[154:155], off
	s_waitcnt vmcnt(8)
	s_waitcnt lgkmcnt(0)
	s_barrier
	v_mfma_f32_16x16x32_bf16 v[64:67], v[138:141], v[188:191], v[64:67]
	v_mfma_f32_16x16x32_bf16 v[60:63], v[146:149], v[188:191], v[60:63]
	v_mfma_f32_16x16x32_bf16 v[48:51], v[138:141], v[196:199], v[48:51]
	v_mfma_f32_16x16x32_bf16 v[44:47], v[146:149], v[196:199], v[44:47]
	v_mfma_f32_16x16x32_bf16 v[32:35], v[138:141], v[222:225], v[32:35]
	v_mfma_f32_16x16x32_bf16 v[28:31], v[146:149], v[222:225], v[28:31]
	v_mfma_f32_16x16x32_bf16 v[16:19], v[138:141], v[230:233], v[16:19]
	v_mfma_f32_16x16x32_bf16 v[12:15], v[146:149], v[230:233], v[12:15]
	v_mfma_f32_16x16x32_bf16 v[64:67], v[142:145], v[192:195], v[64:67]
	v_mfma_f32_16x16x32_bf16 v[60:63], v[150:153], v[192:195], v[60:63]
	v_mfma_f32_16x16x32_bf16 v[48:51], v[142:145], v[200:203], v[48:51]
	v_mfma_f32_16x16x32_bf16 v[44:47], v[150:153], v[200:203], v[44:47]
	v_mfma_f32_16x16x32_bf16 v[32:35], v[142:145], v[226:229], v[32:35]
	v_mfma_f32_16x16x32_bf16 v[28:31], v[150:153], v[226:229], v[28:31]
	v_mfma_f32_16x16x32_bf16 v[16:19], v[142:145], v[234:237], v[16:19]
	v_mfma_f32_16x16x32_bf16 v[12:15], v[150:153], v[234:237], v[12:15]
	v_mfma_f32_16x16x32_bf16 v[56:59], v[168:171], v[188:191], v[56:59]
	v_mfma_f32_16x16x32_bf16 v[52:55], v[176:179], v[188:191], v[52:55]
	v_mfma_f32_16x16x32_bf16 v[40:43], v[168:171], v[196:199], v[40:43]
	v_mfma_f32_16x16x32_bf16 v[36:39], v[176:179], v[196:199], v[36:39]
	v_mfma_f32_16x16x32_bf16 v[24:27], v[168:171], v[222:225], v[24:27]
	v_mfma_f32_16x16x32_bf16 v[20:23], v[176:179], v[222:225], v[20:23]
	v_mfma_f32_16x16x32_bf16 v[8:11], v[168:171], v[230:233], v[8:11]
	v_mfma_f32_16x16x32_bf16 v[4:7], v[176:179], v[230:233], v[4:7]
	v_mfma_f32_16x16x32_bf16 v[56:59], v[172:175], v[192:195], v[56:59]
	v_mfma_f32_16x16x32_bf16 v[52:55], v[180:183], v[192:195], v[52:55]
	v_mfma_f32_16x16x32_bf16 v[40:43], v[172:175], v[200:203], v[40:43]
	v_mfma_f32_16x16x32_bf16 v[36:39], v[180:183], v[200:203], v[36:39]
	v_mfma_f32_16x16x32_bf16 v[24:27], v[172:175], v[226:229], v[24:27]
	v_mfma_f32_16x16x32_bf16 v[20:23], v[180:183], v[226:229], v[20:23]
	v_mfma_f32_16x16x32_bf16 v[8:11], v[172:175], v[234:237], v[8:11]
	v_mfma_f32_16x16x32_bf16 v[4:7], v[180:183], v[234:237], v[4:7]
	s_barrier
	s_add_i32 s58, s58, 2
	s_add_u32 s6, s6, 0x100
	s_addc_u32 s7, s7, 0
	s_add_u32 s21, s21, 0x100
	s_addc_u32 s13, s13, 0
	s_cmp_gt_u32 s58, 61
	s_cbranch_scc0 .LBB0_1202
.LBB0_1202:
	s_add_u32 s24, s6, 0xfff00080
	s_addc_u32 s25, s7, -1
	s_add_i32 s28, 0, 0x10000
	s_cmp_eq_u32 s58, 60
	s_cselect_b32 s27, s35, s25
	s_cselect_b32 s26, s53, s24
	s_cselect_b32 s25, s31, s13
	s_cselect_b32 s24, s92, s21
	s_add_i32 s71, 0, 0x14000
	v_add_u32_e32 v150, s28, v163
	v_add_u32_e32 v154, s71, v163
	ds_read_b128 v[138:141], v150
	ds_read_b128 v[142:145], v150 offset:1024
	ds_read_b128 v[146:149], v150 offset:2048
	ds_read_b128 v[150:153], v150 offset:3072
	ds_read_b128 v[168:171], v154
	ds_read_b128 v[172:175], v154 offset:1024
	ds_read_b128 v[176:179], v154 offset:2048
	ds_read_b128 v[180:183], v154 offset:3072
	v_lshl_add_u64 v[154:155], s[6:7], 0, v[134:135]
	s_add_i32 m0, s50, 0xc000
	ds_read_b128 v[188:191], v186
	ds_read_b128 v[192:195], v186 offset:1024
	ds_read_b128 v[196:199], v186 offset:2048
	ds_read_b128 v[200:203], v186 offset:3072
	ds_read_b128 v[222:225], v186 offset:4096
	ds_read_b128 v[226:229], v186 offset:5120
	ds_read_b128 v[230:233], v186 offset:6144
	ds_read_b128 v[234:237], v186 offset:7168
	global_load_lds_dwordx4 v[154:155], off
	v_lshl_add_u64 v[154:155], s[6:7], 0, v[136:137]
	s_add_i32 m0, s50, 0xe000
	s_nop 0
	global_load_lds_dwordx4 v[154:155], off
	s_waitcnt vmcnt(8)
	s_waitcnt lgkmcnt(0)
	s_barrier
	v_mfma_f32_16x16x32_bf16 v[128:131], v[138:141], v[188:191], v[128:131]
	v_mfma_f32_16x16x32_bf16 v[124:127], v[146:149], v[188:191], v[124:127]
	v_mfma_f32_16x16x32_bf16 v[112:115], v[138:141], v[196:199], v[112:115]
	v_mfma_f32_16x16x32_bf16 v[108:111], v[146:149], v[196:199], v[108:111]
	v_mfma_f32_16x16x32_bf16 v[96:99], v[138:141], v[222:225], v[96:99]
	v_mfma_f32_16x16x32_bf16 v[92:95], v[146:149], v[222:225], v[92:95]
	v_mfma_f32_16x16x32_bf16 v[80:83], v[138:141], v[230:233], v[80:83]
	v_mfma_f32_16x16x32_bf16 v[76:79], v[146:149], v[230:233], v[76:79]
	v_mfma_f32_16x16x32_bf16 v[128:131], v[142:145], v[192:195], v[128:131]
	v_mfma_f32_16x16x32_bf16 v[124:127], v[150:153], v[192:195], v[124:127]
	v_mfma_f32_16x16x32_bf16 v[112:115], v[142:145], v[200:203], v[112:115]
	v_mfma_f32_16x16x32_bf16 v[108:111], v[150:153], v[200:203], v[108:111]
	v_mfma_f32_16x16x32_bf16 v[96:99], v[142:145], v[226:229], v[96:99]
	v_mfma_f32_16x16x32_bf16 v[92:95], v[150:153], v[226:229], v[92:95]
	v_mfma_f32_16x16x32_bf16 v[80:83], v[142:145], v[234:237], v[80:83]
	v_mfma_f32_16x16x32_bf16 v[76:79], v[150:153], v[234:237], v[76:79]
	v_mfma_f32_16x16x32_bf16 v[120:123], v[168:171], v[188:191], v[120:123]
	v_mfma_f32_16x16x32_bf16 v[116:119], v[176:179], v[188:191], v[116:119]
	v_mfma_f32_16x16x32_bf16 v[104:107], v[168:171], v[196:199], v[104:107]
	v_mfma_f32_16x16x32_bf16 v[100:103], v[176:179], v[196:199], v[100:103]
	v_mfma_f32_16x16x32_bf16 v[88:91], v[168:171], v[222:225], v[88:91]
	v_mfma_f32_16x16x32_bf16 v[84:87], v[176:179], v[222:225], v[84:87]
	v_mfma_f32_16x16x32_bf16 v[72:75], v[168:171], v[230:233], v[72:75]
	v_mfma_f32_16x16x32_bf16 v[68:71], v[176:179], v[230:233], v[68:71]
	v_mfma_f32_16x16x32_bf16 v[120:123], v[172:175], v[192:195], v[120:123]
	v_mfma_f32_16x16x32_bf16 v[116:119], v[180:183], v[192:195], v[116:119]
	v_mfma_f32_16x16x32_bf16 v[104:107], v[172:175], v[200:203], v[104:107]
	v_mfma_f32_16x16x32_bf16 v[100:103], v[180:183], v[200:203], v[100:103]
	v_mfma_f32_16x16x32_bf16 v[88:91], v[172:175], v[226:229], v[88:91]
	v_mfma_f32_16x16x32_bf16 v[84:87], v[180:183], v[226:229], v[84:87]
	v_mfma_f32_16x16x32_bf16 v[72:75], v[172:175], v[234:237], v[72:75]
	v_mfma_f32_16x16x32_bf16 v[68:71], v[180:183], v[234:237], v[68:71]
	s_barrier
	s_add_i32 s28, s28, s46
	v_lshl_add_u64 v[154:155], s[24:25], 0, v[2:3]
	s_mov_b32 m0, s28
	ds_read_b128 v[188:191], v186 offset:16384
	ds_read_b128 v[192:195], v186 offset:17408
	ds_read_b128 v[196:199], v186 offset:18432
	ds_read_b128 v[200:203], v186 offset:19456
	ds_read_b128 v[222:225], v186 offset:20480
	ds_read_b128 v[226:229], v186 offset:21504
	ds_read_b128 v[230:233], v186 offset:22528
	ds_read_b128 v[234:237], v186 offset:23552
	global_load_lds_dwordx4 v[154:155], off
	s_add_i32 m0, s28, 0x2000
	s_add_u32 s28, s24, 0x100000
	v_lshl_add_u64 v[184:185], s[24:25], 0, v[132:133]
	s_addc_u32 s29, s25, 0
	s_add_i32 s71, s71, s46
	global_load_lds_dwordx4 v[184:185], off
	v_lshl_add_u64 v[204:205], s[28:29], 0, v[2:3]
	s_mov_b32 m0, s71
	v_lshl_add_u64 v[238:239], s[26:27], 0, v[132:133]
	global_load_lds_dwordx4 v[204:205], off
	v_lshl_add_u64 v[204:205], s[28:29], 0, v[132:133]
	s_add_i32 m0, s71, 0x2000
	s_nop 0
	global_load_lds_dwordx4 v[204:205], off
	v_lshl_add_u64 v[204:205], s[26:27], 0, v[2:3]
	s_mov_b32 m0, s50
	s_nop 0
	global_load_lds_dwordx4 v[204:205], off
	s_mov_b32 m0, s23
	s_nop 0
	global_load_lds_dwordx4 v[238:239], off
	s_waitcnt vmcnt(8)
	s_waitcnt lgkmcnt(0)
	s_barrier
	v_mfma_f32_16x16x32_bf16 v[64:67], v[138:141], v[188:191], v[64:67]
	v_mfma_f32_16x16x32_bf16 v[60:63], v[146:149], v[188:191], v[60:63]
	v_mfma_f32_16x16x32_bf16 v[48:51], v[138:141], v[196:199], v[48:51]
	v_mfma_f32_16x16x32_bf16 v[44:47], v[146:149], v[196:199], v[44:47]
	v_mfma_f32_16x16x32_bf16 v[32:35], v[138:141], v[222:225], v[32:35]
	v_mfma_f32_16x16x32_bf16 v[28:31], v[146:149], v[222:225], v[28:31]
	v_mfma_f32_16x16x32_bf16 v[16:19], v[138:141], v[230:233], v[16:19]
	v_mfma_f32_16x16x32_bf16 v[12:15], v[146:149], v[230:233], v[12:15]
	v_mfma_f32_16x16x32_bf16 v[64:67], v[142:145], v[192:195], v[64:67]
	v_mfma_f32_16x16x32_bf16 v[60:63], v[150:153], v[192:195], v[60:63]
	v_mfma_f32_16x16x32_bf16 v[48:51], v[142:145], v[200:203], v[48:51]
	v_mfma_f32_16x16x32_bf16 v[44:47], v[150:153], v[200:203], v[44:47]
	v_mfma_f32_16x16x32_bf16 v[32:35], v[142:145], v[226:229], v[32:35]
	v_mfma_f32_16x16x32_bf16 v[28:31], v[150:153], v[226:229], v[28:31]
	v_mfma_f32_16x16x32_bf16 v[16:19], v[142:145], v[234:237], v[16:19]
	v_mfma_f32_16x16x32_bf16 v[12:15], v[150:153], v[234:237], v[12:15]
	v_mfma_f32_16x16x32_bf16 v[56:59], v[168:171], v[188:191], v[56:59]
	v_mfma_f32_16x16x32_bf16 v[52:55], v[176:179], v[188:191], v[52:55]
	v_mfma_f32_16x16x32_bf16 v[40:43], v[168:171], v[196:199], v[40:43]
	v_mfma_f32_16x16x32_bf16 v[36:39], v[176:179], v[196:199], v[36:39]
	v_mfma_f32_16x16x32_bf16 v[24:27], v[168:171], v[222:225], v[24:27]
	v_mfma_f32_16x16x32_bf16 v[20:23], v[176:179], v[222:225], v[20:23]
	v_mfma_f32_16x16x32_bf16 v[8:11], v[168:171], v[230:233], v[8:11]
	v_mfma_f32_16x16x32_bf16 v[4:7], v[176:179], v[230:233], v[4:7]
	v_mfma_f32_16x16x32_bf16 v[56:59], v[172:175], v[192:195], v[56:59]
	v_mfma_f32_16x16x32_bf16 v[52:55], v[180:183], v[192:195], v[52:55]
	v_mfma_f32_16x16x32_bf16 v[40:43], v[172:175], v[200:203], v[40:43]
	v_mfma_f32_16x16x32_bf16 v[36:39], v[180:183], v[200:203], v[36:39]
	v_mfma_f32_16x16x32_bf16 v[24:27], v[172:175], v[226:229], v[24:27]
	v_mfma_f32_16x16x32_bf16 v[20:23], v[180:183], v[226:229], v[20:23]
	v_mfma_f32_16x16x32_bf16 v[8:11], v[172:175], v[234:237], v[8:11]
	v_mfma_f32_16x16x32_bf16 v[4:7], v[180:183], v[234:237], v[4:7]
	s_barrier
	s_add_i32 s28, 0, 0x18000
	s_add_i32 s29, 0, 0x1c000
	v_add_u32_e32 v150, s28, v163
	v_add_u32_e32 v180, s29, v163
	ds_read_b128 v[138:141], v150
	ds_read_b128 v[142:145], v150 offset:1024
	ds_read_b128 v[146:149], v150 offset:2048
	ds_read_b128 v[150:153], v150 offset:3072
	ds_read_b128 v[168:171], v180
	ds_read_b128 v[172:175], v180 offset:1024
	ds_read_b128 v[176:179], v180 offset:2048
	ds_read_b128 v[180:183], v180 offset:3072
	s_add_u32 s26, s26, 0x100000
	s_addc_u32 s27, s27, 0
	s_mov_b32 m0, s51
	v_lshl_add_u64 v[240:241], s[26:27], 0, v[2:3]
	ds_read_b128 v[188:191], v186 offset:32768
	ds_read_b128 v[192:195], v186 offset:33792
	ds_read_b128 v[196:199], v186 offset:34816
	ds_read_b128 v[200:203], v186 offset:35840
	ds_read_b128 v[222:225], v186 offset:36864
	ds_read_b128 v[226:229], v186 offset:37888
	ds_read_b128 v[230:233], v186 offset:38912
	ds_read_b128 v[234:237], v186 offset:39936
	global_load_lds_dwordx4 v[240:241], off
	v_lshl_add_u64 v[240:241], s[26:27], 0, v[132:133]
	s_mov_b32 m0, s54
	s_nop 0
	global_load_lds_dwordx4 v[240:241], off
	s_waitcnt vmcnt(8)
	s_waitcnt lgkmcnt(0)
	s_barrier
	v_mfma_f32_16x16x32_bf16 v[128:131], v[138:141], v[188:191], v[128:131]
	v_mfma_f32_16x16x32_bf16 v[124:127], v[146:149], v[188:191], v[124:127]
	v_mfma_f32_16x16x32_bf16 v[112:115], v[138:141], v[196:199], v[112:115]
	v_mfma_f32_16x16x32_bf16 v[108:111], v[146:149], v[196:199], v[108:111]
	v_mfma_f32_16x16x32_bf16 v[96:99], v[138:141], v[222:225], v[96:99]
	v_mfma_f32_16x16x32_bf16 v[92:95], v[146:149], v[222:225], v[92:95]
	v_mfma_f32_16x16x32_bf16 v[80:83], v[138:141], v[230:233], v[80:83]
	v_mfma_f32_16x16x32_bf16 v[76:79], v[146:149], v[230:233], v[76:79]
	v_mfma_f32_16x16x32_bf16 v[128:131], v[142:145], v[192:195], v[128:131]
	v_mfma_f32_16x16x32_bf16 v[124:127], v[150:153], v[192:195], v[124:127]
	v_mfma_f32_16x16x32_bf16 v[112:115], v[142:145], v[200:203], v[112:115]
	v_mfma_f32_16x16x32_bf16 v[108:111], v[150:153], v[200:203], v[108:111]
	v_mfma_f32_16x16x32_bf16 v[96:99], v[142:145], v[226:229], v[96:99]
	v_mfma_f32_16x16x32_bf16 v[92:95], v[150:153], v[226:229], v[92:95]
	v_mfma_f32_16x16x32_bf16 v[80:83], v[142:145], v[234:237], v[80:83]
	v_mfma_f32_16x16x32_bf16 v[76:79], v[150:153], v[234:237], v[76:79]
	v_mfma_f32_16x16x32_bf16 v[120:123], v[168:171], v[188:191], v[120:123]
	v_mfma_f32_16x16x32_bf16 v[116:119], v[176:179], v[188:191], v[116:119]
	v_mfma_f32_16x16x32_bf16 v[104:107], v[168:171], v[196:199], v[104:107]
	v_mfma_f32_16x16x32_bf16 v[100:103], v[176:179], v[196:199], v[100:103]
	v_mfma_f32_16x16x32_bf16 v[88:91], v[168:171], v[222:225], v[88:91]
	v_mfma_f32_16x16x32_bf16 v[84:87], v[176:179], v[222:225], v[84:87]
	v_mfma_f32_16x16x32_bf16 v[72:75], v[168:171], v[230:233], v[72:75]
	v_mfma_f32_16x16x32_bf16 v[68:71], v[176:179], v[230:233], v[68:71]
	v_mfma_f32_16x16x32_bf16 v[120:123], v[172:175], v[192:195], v[120:123]
	v_mfma_f32_16x16x32_bf16 v[116:119], v[180:183], v[192:195], v[116:119]
	v_mfma_f32_16x16x32_bf16 v[104:107], v[172:175], v[200:203], v[104:107]
	v_mfma_f32_16x16x32_bf16 v[100:103], v[180:183], v[200:203], v[100:103]
	v_mfma_f32_16x16x32_bf16 v[88:91], v[172:175], v[226:229], v[88:91]
	v_mfma_f32_16x16x32_bf16 v[84:87], v[180:183], v[226:229], v[84:87]
	v_mfma_f32_16x16x32_bf16 v[72:75], v[172:175], v[234:237], v[72:75]
	v_mfma_f32_16x16x32_bf16 v[68:71], v[180:183], v[234:237], v[68:71]
	s_barrier
	s_add_i32 s26, s28, s46
	v_lshl_add_u64 v[154:155], v[154:155], 0, s[86:87]
	s_mov_b32 m0, s26
	ds_read_b128 v[188:191], v186 offset:49152
	ds_read_b128 v[192:195], v186 offset:50176
	ds_read_b128 v[196:199], v186 offset:51200
	ds_read_b128 v[200:203], v186 offset:52224
	ds_read_b128 v[222:225], v186 offset:53248
	ds_read_b128 v[226:229], v186 offset:54272
	ds_read_b128 v[230:233], v186 offset:55296
	ds_read_b128 v[234:237], v186 offset:56320
	global_load_lds_dwordx4 v[154:155], off
	s_add_i32 m0, s26, 0x2000
	s_add_u32 s24, s24, 0x100080
	v_lshl_add_u64 v[154:155], v[184:185], 0, s[86:87]
	s_addc_u32 s25, s25, 0
	s_add_i32 s26, s29, s46
	global_load_lds_dwordx4 v[154:155], off
	v_lshl_add_u64 v[154:155], s[24:25], 0, v[2:3]
	s_mov_b32 m0, s26
	s_nop 0
	global_load_lds_dwordx4 v[154:155], off
	v_lshl_add_u64 v[154:155], s[24:25], 0, v[132:133]
	s_add_i32 m0, s26, 0x2000
	s_nop 0
	global_load_lds_dwordx4 v[154:155], off
	v_lshl_add_u64 v[154:155], v[204:205], 0, s[86:87]
	s_mov_b32 m0, s76
	s_nop 0
	global_load_lds_dwordx4 v[154:155], off
	v_lshl_add_u64 v[154:155], v[238:239], 0, s[86:87]
	s_mov_b32 m0, s77
	s_nop 0
	global_load_lds_dwordx4 v[154:155], off
	s_waitcnt vmcnt(8)
	s_waitcnt lgkmcnt(0)
	s_barrier
	v_mfma_f32_16x16x32_bf16 v[64:67], v[138:141], v[188:191], v[64:67]
	v_mfma_f32_16x16x32_bf16 v[60:63], v[146:149], v[188:191], v[60:63]
	v_mfma_f32_16x16x32_bf16 v[48:51], v[138:141], v[196:199], v[48:51]
	v_mfma_f32_16x16x32_bf16 v[44:47], v[146:149], v[196:199], v[44:47]
	v_mfma_f32_16x16x32_bf16 v[32:35], v[138:141], v[222:225], v[32:35]
	v_mfma_f32_16x16x32_bf16 v[28:31], v[146:149], v[222:225], v[28:31]
	v_mfma_f32_16x16x32_bf16 v[16:19], v[138:141], v[230:233], v[16:19]
	v_mfma_f32_16x16x32_bf16 v[12:15], v[146:149], v[230:233], v[12:15]
	v_mfma_f32_16x16x32_bf16 v[64:67], v[142:145], v[192:195], v[64:67]
	v_mfma_f32_16x16x32_bf16 v[60:63], v[150:153], v[192:195], v[60:63]
	v_mfma_f32_16x16x32_bf16 v[48:51], v[142:145], v[200:203], v[48:51]
	v_mfma_f32_16x16x32_bf16 v[44:47], v[150:153], v[200:203], v[44:47]
	v_mfma_f32_16x16x32_bf16 v[32:35], v[142:145], v[226:229], v[32:35]
	v_mfma_f32_16x16x32_bf16 v[28:31], v[150:153], v[226:229], v[28:31]
	v_mfma_f32_16x16x32_bf16 v[16:19], v[142:145], v[234:237], v[16:19]
	v_mfma_f32_16x16x32_bf16 v[12:15], v[150:153], v[234:237], v[12:15]
	v_mfma_f32_16x16x32_bf16 v[56:59], v[168:171], v[188:191], v[56:59]
	v_mfma_f32_16x16x32_bf16 v[52:55], v[176:179], v[188:191], v[52:55]
	v_mfma_f32_16x16x32_bf16 v[40:43], v[168:171], v[196:199], v[40:43]
	v_mfma_f32_16x16x32_bf16 v[36:39], v[176:179], v[196:199], v[36:39]
	v_mfma_f32_16x16x32_bf16 v[24:27], v[168:171], v[222:225], v[24:27]
	v_mfma_f32_16x16x32_bf16 v[20:23], v[176:179], v[222:225], v[20:23]
	v_mfma_f32_16x16x32_bf16 v[8:11], v[168:171], v[230:233], v[8:11]
	v_mfma_f32_16x16x32_bf16 v[4:7], v[176:179], v[230:233], v[4:7]
	v_mfma_f32_16x16x32_bf16 v[56:59], v[172:175], v[192:195], v[56:59]
	v_mfma_f32_16x16x32_bf16 v[52:55], v[180:183], v[192:195], v[52:55]
	v_mfma_f32_16x16x32_bf16 v[40:43], v[172:175], v[200:203], v[40:43]
	v_mfma_f32_16x16x32_bf16 v[36:39], v[180:183], v[200:203], v[36:39]
	v_mfma_f32_16x16x32_bf16 v[24:27], v[172:175], v[226:229], v[24:27]
	v_mfma_f32_16x16x32_bf16 v[20:23], v[180:183], v[226:229], v[20:23]
	v_mfma_f32_16x16x32_bf16 v[8:11], v[172:175], v[234:237], v[8:11]
	v_mfma_f32_16x16x32_bf16 v[4:7], v[180:183], v[234:237], v[4:7]
	s_barrier
	s_add_i32 s58, s58, 2
	s_add_u32 s6, s6, 0x100
	s_addc_u32 s7, s7, 0
	s_add_u32 s21, s21, 0x100
	s_addc_u32 s13, s13, 0
	s_cmp_gt_u32 s58, 61
	s_cbranch_scc0 .LBB0_1202
	s_setprio 0
	s_and_b64 vcc, exec, s[14:15]
	s_cbranch_vccz .LBB0_1205
	s_barrier
